# speedup vs baseline: 1.3095x; 1.3095x over previous
.LBB0_78:
	s_load_dwordx2 s[0:1], s[0:1], 0x28
	v_lshlrev_b32_e32 v2, 9, v0
	v_and_b32_e32 v13, 3, v0
	v_and_b32_e32 v2, 0x7800, v2
	v_mov_b32_e32 v3, 0
	v_lshl_or_b32 v12, s36, 2, v13
	s_waitcnt lgkmcnt(0)
	s_mov_b64 s[44:45], s[0:1]
	v_and_b32_e32 v164, 15, v0
	v_lshlrev_b32_e32 v164, 2, v164
	v_add_u32_e32 v164, 0x14a80, v164
	v_mov_b32_e32 v165, 0
	ds_write_b32 v164, v165
	v_lshl_add_u64 v[4:5], s[0:1], 0, v[2:3]
	s_lshl_b32 s0, s33, 7
	v_lshl_or_b32 v2, v12, 3, s0
	v_lshl_add_u64 v[10:11], v[4:5], 0, v[2:3]
	v_and_b32_e32 v160, 15, v0
	v_bfe_u32 v161, v0, 4, 2
	s_and_b32 s46, s36, 1
	s_lshl_b32 s46, s46, 5
	v_lshl_add_u32 v162, v161, 3, s46
	v_lshlrev_b32_e32 v162, 7, v162
	s_lshl_b32 s47, s33, 5
	s_lshr_b32 s46, s36, 1
	s_add_i32 s47, s47, s46
	v_lshl_add_u32 v163, v160, 1, s47
	v_add_lshl_u32 v162, v162, v163, 2
	global_load_dword v152, v162, s[44:45]
	global_load_dword v153, v162, s[44:45] offset:512
	global_load_dword v154, v162, s[44:45] offset:1024
	global_load_dword v155, v162, s[44:45] offset:1536
	global_load_dword v156, v162, s[44:45] offset:2048
	global_load_dword v157, v162, s[44:45] offset:2560
	global_load_dword v158, v162, s[44:45] offset:3072
	global_load_dword v159, v162, s[44:45] offset:3584
	s_bfe_u32 s5, s2, 0x30002
	s_mov_b32 s4, 2
	s_cmp_gt_u32 s5, 3
	v_lshlrev_b32_e32 v10, 2, v0
	s_cbranch_scc0 .LBB0_80
	v_and_b32_e32 v11, 16, v10
	v_lshl_or_b32 v14, s5, 5, v11
	s_cbranch_execz .LBB0_81
	s_branch .LBB0_82

.LBB0_86:
	s_or_b64 exec, exec, s[0:1]
	v_cmp_ne_u32_e32 vcc, 0, v14
	s_waitcnt lgkmcnt(0)
	s_barrier
	s_setprio 2
	v_and_b32_e32 v40, 15, v1
	v_lshrrev_b32_e32 v41, 4, v1
	s_and_b32 s44, s36, 1
	s_lshr_b32 s45, s36, 1
	s_mov_b32 s60, 0xffff
	s_mov_b32 s61, 0
	s_mov_b32 s62, 0xffff0000
	s_mov_b32 s63, 0
	s_mov_b32 s64, 0
	s_mov_b32 s65, 0xffff
	s_mov_b32 s66, 0
	s_mov_b32 s67, 0xffff0000
	v_cvt_pk_f16_f32 v2, v152, v153
	v_cvt_pk_f16_f32 v3, v154, v155
	v_cvt_pk_f16_f32 v4, v156, v157
	v_cvt_pk_f16_f32 v5, v158, v159
	s_lshl_b32 s46, s44, 3
	v_lshl_add_u32 v42, v41, 1, s46
	v_mul_u32_u24_e32 v32, 0x650, v42
	v_lshl_add_u32 v34, v40, 3, v32
	v_mul_u32_u24_e32 v33, 0x650, v40
	v_add_u32_e32 v33, 0x6500, v33
	s_lshl_b32 s47, s45, 1
	s_lshl_b32 s46, s44, 10
	s_add_i32 s47, s47, s46
	s_add_i32 s47, s47, 0x14b00
	v_lshl_add_u32 v39, v40, 2, s47
	v_lshl_add_u32 v39, v41, 8, v39
	v_lshlrev_b32_e32 v43, 4, v1
	v_add_u32_e32 v43, 0x14b00, v43
	v_lshlrev_b32_e32 v35, 4, v1
	v_mov_b32_e32 v44, 1
	s_lshl_b32 s46, s3, 2
	s_add_i32 s46, s46, s33
	s_mul_i32 s46, s46, 0x3200
	s_add_u32 s68, s26, s46
	s_addc_u32 s69, s27, 0
	s_mov_b32 s73, 0
	v_mov_b32_e32 v36, 0x14a00
.Lc_wait0:
	ds_read_b32 v37, v36
	ds_read_b32 v38, v36 offset:64
	s_waitcnt lgkmcnt(0)
	v_readfirstlane_b32 s4, v37
	v_readfirstlane_b32 s5, v38
	s_and_b32 s4, s4, s5
	s_cbranch_scc1 .Lc_go
	s_sleep 1
	s_add_i32 s73, s73, 1
	s_cmp_lt_u32 s73, 0x4000
	s_cbranch_scc1 .Lc_wait0
.Lc_go:
	s_cmp_eq_u32 s45, 0
	s_cbranch_scc0 .Lc_par1
	ds_read2_b64 v[48:51], v32 offset0:0 offset1:202
	ds_read_b128 v[120:123], v33 offset:0
	ds_read2_b64 v[10:13], v34 offset0:0 offset1:202
	ds_read2_b64 v[52:55], v32 offset0:1 offset1:203
	ds_read2_b64 v[56:59], v32 offset0:2 offset1:204
	ds_read_b128 v[124:127], v33 offset:16
	ds_read2_b64 v[60:63], v32 offset0:3 offset1:205
	ds_read2_b64 v[64:67], v32 offset0:4 offset1:206
	ds_read_b128 v[128:131], v33 offset:32
	ds_read2_b64 v[68:71], v32 offset0:5 offset1:207
	s_mov_b32 s70, 0
	s_mov_b32 s71, 0
.Lc0_loop:
	s_waitcnt lgkmcnt(6)
	v_pk_fma_f16 v6, v2, v120, v121 op_sel:[0,0,0] op_sel_hi:[1,0,0] neg_lo:[1,0,0] neg_hi:[1,0,0]
	v_pk_fma_f16 v7, v3, v120, v121 op_sel:[0,0,0] op_sel_hi:[1,0,0] neg_lo:[1,0,0] neg_hi:[1,0,0]
	v_pk_fma_f16 v8, v4, v120, v121 op_sel:[0,0,0] op_sel_hi:[1,0,0] neg_lo:[1,0,0] neg_hi:[1,0,0]
	v_pk_fma_f16 v9, v5, v120, v121 op_sel:[0,0,0] op_sel_hi:[1,0,0] neg_lo:[1,0,0] neg_hi:[1,0,0]
	v_mfma_f32_16x16x32_f16 v[18:21], v[10:13], v[2:5], 0
	ds_read2_b64 v[72:75], v32 offset0:6 offset1:208
	ds_read_b128 v[132:135], v33 offset:48
	ds_read_b32 v37, v36 offset:4
	ds_read_b32 v38, v36 offset:68
	v_pk_fma_f16 v2, v48, v6, v2
	v_pk_fma_f16 v3, v49, v7, v3
	v_pk_fma_f16 v4, v50, v8, v4
	v_pk_fma_f16 v5, v51, v9, v5
	v_cndmask_b32_e64 v29, v29, v25, s[66:67]
	v_cvt_pk_f16_f32 v30, v26, v27
	v_cvt_pk_f16_f32 v31, v28, v29
	ds_write_b16 v39, v30 offset:0
	ds_write_b16_d16_hi v39, v30 offset:64
	ds_write_b16 v39, v31 offset:128
	ds_write_b16_d16_hi v39, v31 offset:192
	s_mov_b64 exec, 1
	ds_add_u32 v36, v44 offset:124
	s_mov_b64 exec, -1
	v_pk_fma_f16 v6, v2, v122, v123 op_sel:[0,0,0] op_sel_hi:[1,0,0] neg_lo:[1,0,0] neg_hi:[1,0,0]
	v_pk_fma_f16 v7, v3, v122, v123 op_sel:[0,0,0] op_sel_hi:[1,0,0] neg_lo:[1,0,0] neg_hi:[1,0,0]
	v_pk_fma_f16 v8, v4, v122, v123 op_sel:[0,0,0] op_sel_hi:[1,0,0] neg_lo:[1,0,0] neg_hi:[1,0,0]
	v_pk_fma_f16 v9, v5, v122, v123 op_sel:[0,0,0] op_sel_hi:[1,0,0] neg_lo:[1,0,0] neg_hi:[1,0,0]
	v_mfma_f32_16x16x32_f16 v[22:25], v[10:13], v[2:5], 0
	ds_read2_b64 v[76:79], v32 offset0:7 offset1:209
	v_pk_fma_f16 v2, v52, v6, v2
	v_pk_fma_f16 v3, v53, v7, v3
	v_pk_fma_f16 v4, v54, v8, v4
	v_pk_fma_f16 v5, v55, v9, v5
	v_cndmask_b32_e64 v26, v26, v18, s[60:61]
	s_waitcnt lgkmcnt(13)
	v_pk_fma_f16 v6, v2, v124, v125 op_sel:[0,0,0] op_sel_hi:[1,0,0] neg_lo:[1,0,0] neg_hi:[1,0,0]
	v_pk_fma_f16 v7, v3, v124, v125 op_sel:[0,0,0] op_sel_hi:[1,0,0] neg_lo:[1,0,0] neg_hi:[1,0,0]
	v_pk_fma_f16 v8, v4, v124, v125 op_sel:[0,0,0] op_sel_hi:[1,0,0] neg_lo:[1,0,0] neg_hi:[1,0,0]
	v_pk_fma_f16 v9, v5, v124, v125 op_sel:[0,0,0] op_sel_hi:[1,0,0] neg_lo:[1,0,0] neg_hi:[1,0,0]
	v_mfma_f32_16x16x32_f16 v[18:21], v[10:13], v[2:5], 0
	ds_read2_b64 v[80:83], v32 offset0:8 offset1:210
	ds_read_b128 v[136:139], v33 offset:64
	v_pk_fma_f16 v2, v56, v6, v2
	v_pk_fma_f16 v3, v57, v7, v3
	v_pk_fma_f16 v4, v58, v8, v4
	v_pk_fma_f16 v5, v59, v9, v5
	v_cndmask_b32_e64 v27, v27, v23, s[60:61]
	v_pk_fma_f16 v6, v2, v126, v127 op_sel:[0,0,0] op_sel_hi:[1,0,0] neg_lo:[1,0,0] neg_hi:[1,0,0]
	v_pk_fma_f16 v7, v3, v126, v127 op_sel:[0,0,0] op_sel_hi:[1,0,0] neg_lo:[1,0,0] neg_hi:[1,0,0]
	v_pk_fma_f16 v8, v4, v126, v127 op_sel:[0,0,0] op_sel_hi:[1,0,0] neg_lo:[1,0,0] neg_hi:[1,0,0]
	v_pk_fma_f16 v9, v5, v126, v127 op_sel:[0,0,0] op_sel_hi:[1,0,0] neg_lo:[1,0,0] neg_hi:[1,0,0]
	v_mfma_f32_16x16x32_f16 v[22:25], v[10:13], v[2:5], 0
	ds_read2_b64 v[84:87], v32 offset0:9 offset1:211
	v_pk_fma_f16 v2, v60, v6, v2
	v_pk_fma_f16 v3, v61, v7, v3
	v_pk_fma_f16 v4, v62, v8, v4
	v_pk_fma_f16 v5, v63, v9, v5
	v_cndmask_b32_e64 v28, v28, v20, s[60:61]
	s_waitcnt lgkmcnt(13)
	v_pk_fma_f16 v6, v2, v128, v129 op_sel:[0,0,0] op_sel_hi:[1,0,0] neg_lo:[1,0,0] neg_hi:[1,0,0]
	v_pk_fma_f16 v7, v3, v128, v129 op_sel:[0,0,0] op_sel_hi:[1,0,0] neg_lo:[1,0,0] neg_hi:[1,0,0]
	v_pk_fma_f16 v8, v4, v128, v129 op_sel:[0,0,0] op_sel_hi:[1,0,0] neg_lo:[1,0,0] neg_hi:[1,0,0]
	v_pk_fma_f16 v9, v5, v128, v129 op_sel:[0,0,0] op_sel_hi:[1,0,0] neg_lo:[1,0,0] neg_hi:[1,0,0]
	v_mfma_f32_16x16x32_f16 v[18:21], v[10:13], v[2:5], 0
	ds_read2_b64 v[88:91], v32 offset0:10 offset1:212
	ds_read_b128 v[140:143], v33 offset:80
	v_pk_fma_f16 v2, v64, v6, v2
	v_pk_fma_f16 v3, v65, v7, v3
	v_pk_fma_f16 v4, v66, v8, v4
	v_pk_fma_f16 v5, v67, v9, v5
	v_cndmask_b32_e64 v29, v29, v25, s[60:61]
	v_pk_fma_f16 v6, v2, v130, v131 op_sel:[0,0,0] op_sel_hi:[1,0,0] neg_lo:[1,0,0] neg_hi:[1,0,0]
	v_pk_fma_f16 v7, v3, v130, v131 op_sel:[0,0,0] op_sel_hi:[1,0,0] neg_lo:[1,0,0] neg_hi:[1,0,0]
	v_pk_fma_f16 v8, v4, v130, v131 op_sel:[0,0,0] op_sel_hi:[1,0,0] neg_lo:[1,0,0] neg_hi:[1,0,0]
	v_pk_fma_f16 v9, v5, v130, v131 op_sel:[0,0,0] op_sel_hi:[1,0,0] neg_lo:[1,0,0] neg_hi:[1,0,0]
	v_mfma_f32_16x16x32_f16 v[22:25], v[10:13], v[2:5], 0
	ds_read2_b64 v[92:95], v32 offset0:11 offset1:213
	v_pk_fma_f16 v2, v68, v6, v2
	v_pk_fma_f16 v3, v69, v7, v3
	v_pk_fma_f16 v4, v70, v8, v4
	v_pk_fma_f16 v5, v71, v9, v5
	v_cndmask_b32_e64 v26, v26, v18, s[62:63]
	s_waitcnt lgkmcnt(6)
	v_pk_fma_f16 v6, v2, v132, v133 op_sel:[0,0,0] op_sel_hi:[1,0,0] neg_lo:[1,0,0] neg_hi:[1,0,0]
	v_pk_fma_f16 v7, v3, v132, v133 op_sel:[0,0,0] op_sel_hi:[1,0,0] neg_lo:[1,0,0] neg_hi:[1,0,0]
	v_pk_fma_f16 v8, v4, v132, v133 op_sel:[0,0,0] op_sel_hi:[1,0,0] neg_lo:[1,0,0] neg_hi:[1,0,0]
	v_pk_fma_f16 v9, v5, v132, v133 op_sel:[0,0,0] op_sel_hi:[1,0,0] neg_lo:[1,0,0] neg_hi:[1,0,0]
	v_mfma_f32_16x16x32_f16 v[18:21], v[10:13], v[2:5], 0
	ds_read2_b64 v[96:99], v32 offset0:12 offset1:214
	ds_read_b128 v[144:147], v33 offset:96
	v_pk_fma_f16 v2, v72, v6, v2
	v_pk_fma_f16 v3, v73, v7, v3
	v_pk_fma_f16 v4, v74, v8, v4
	v_pk_fma_f16 v5, v75, v9, v5
	v_cndmask_b32_e64 v27, v27, v23, s[62:63]
	v_pk_fma_f16 v6, v2, v134, v135 op_sel:[0,0,0] op_sel_hi:[1,0,0] neg_lo:[1,0,0] neg_hi:[1,0,0]
	v_pk_fma_f16 v7, v3, v134, v135 op_sel:[0,0,0] op_sel_hi:[1,0,0] neg_lo:[1,0,0] neg_hi:[1,0,0]
	v_pk_fma_f16 v8, v4, v134, v135 op_sel:[0,0,0] op_sel_hi:[1,0,0] neg_lo:[1,0,0] neg_hi:[1,0,0]
	v_pk_fma_f16 v9, v5, v134, v135 op_sel:[0,0,0] op_sel_hi:[1,0,0] neg_lo:[1,0,0] neg_hi:[1,0,0]
	v_mfma_f32_16x16x32_f16 v[22:25], v[10:13], v[2:5], 0
	ds_read2_b64 v[100:103], v32 offset0:13 offset1:215
	v_pk_fma_f16 v2, v76, v6, v2
	v_pk_fma_f16 v3, v77, v7, v3
	v_pk_fma_f16 v4, v78, v8, v4
	v_pk_fma_f16 v5, v79, v9, v5
	v_cndmask_b32_e64 v28, v28, v20, s[62:63]
	s_waitcnt lgkmcnt(6)
	v_pk_fma_f16 v6, v2, v136, v137 op_sel:[0,0,0] op_sel_hi:[1,0,0] neg_lo:[1,0,0] neg_hi:[1,0,0]
	v_pk_fma_f16 v7, v3, v136, v137 op_sel:[0,0,0] op_sel_hi:[1,0,0] neg_lo:[1,0,0] neg_hi:[1,0,0]
	v_pk_fma_f16 v8, v4, v136, v137 op_sel:[0,0,0] op_sel_hi:[1,0,0] neg_lo:[1,0,0] neg_hi:[1,0,0]
	v_pk_fma_f16 v9, v5, v136, v137 op_sel:[0,0,0] op_sel_hi:[1,0,0] neg_lo:[1,0,0] neg_hi:[1,0,0]
	v_mfma_f32_16x16x32_f16 v[18:21], v[10:13], v[2:5], 0
	ds_read2_b64 v[104:107], v32 offset0:14 offset1:216
	ds_read_b128 v[148:151], v33 offset:112
	v_pk_fma_f16 v2, v80, v6, v2
	v_pk_fma_f16 v3, v81, v7, v3
	v_pk_fma_f16 v4, v82, v8, v4
	v_pk_fma_f16 v5, v83, v9, v5
	v_cndmask_b32_e64 v29, v29, v25, s[62:63]
	v_readfirstlane_b32 s4, v37
	v_readfirstlane_b32 s5, v38
	s_and_b32 s4, s4, s5
	s_cbranch_scc0 .Lc0_slow0
.Lc0_back0:
	s_mov_b32 s72, 0
	s_cmp_eq_u32 s70, 0
	s_cbranch_scc1 .Lc0_nd0
	s_sub_i32 s4, 3, s71
	s_cmp_eq_u32 s36, s4
	s_cbranch_scc0 .Lc0_nd0
	s_mov_b32 s72, 1
	ds_read_b32 v45, v36 offset:124
	ds_read_b128 v[112:115], v43 offset:0
	ds_read_b128 v[116:119], v43 offset:1024
.Lc0_nd0:
	v_pk_fma_f16 v6, v2, v138, v139 op_sel:[0,0,0] op_sel_hi:[1,0,0] neg_lo:[1,0,0] neg_hi:[1,0,0]
	v_pk_fma_f16 v7, v3, v138, v139 op_sel:[0,0,0] op_sel_hi:[1,0,0] neg_lo:[1,0,0] neg_hi:[1,0,0]
	v_pk_fma_f16 v8, v4, v138, v139 op_sel:[0,0,0] op_sel_hi:[1,0,0] neg_lo:[1,0,0] neg_hi:[1,0,0]
	v_pk_fma_f16 v9, v5, v138, v139 op_sel:[0,0,0] op_sel_hi:[1,0,0] neg_lo:[1,0,0] neg_hi:[1,0,0]
	v_mfma_f32_16x16x32_f16 v[22:25], v[10:13], v[2:5], 0
	ds_read2_b64 v[108:111], v32 offset0:15 offset1:217
	v_pk_fma_f16 v2, v84, v6, v2
	v_pk_fma_f16 v3, v85, v7, v3
	v_pk_fma_f16 v4, v86, v8, v4
	v_pk_fma_f16 v5, v87, v9, v5
	v_cndmask_b32_e64 v26, v26, v18, s[64:65]
	s_waitcnt lgkmcnt(6)
	v_pk_fma_f16 v6, v2, v140, v141 op_sel:[0,0,0] op_sel_hi:[1,0,0] neg_lo:[1,0,0] neg_hi:[1,0,0]
	v_pk_fma_f16 v7, v3, v140, v141 op_sel:[0,0,0] op_sel_hi:[1,0,0] neg_lo:[1,0,0] neg_hi:[1,0,0]
	v_pk_fma_f16 v8, v4, v140, v141 op_sel:[0,0,0] op_sel_hi:[1,0,0] neg_lo:[1,0,0] neg_hi:[1,0,0]
	v_pk_fma_f16 v9, v5, v140, v141 op_sel:[0,0,0] op_sel_hi:[1,0,0] neg_lo:[1,0,0] neg_hi:[1,0,0]
	v_mfma_f32_16x16x32_f16 v[18:21], v[10:13], v[2:5], 0
	ds_read2_b64 v[48:51], v32 offset0:16 offset1:218
	ds_read_b128 v[120:123], v33 offset:128
	ds_read2_b64 v[14:17], v34 offset0:16 offset1:218
	v_pk_fma_f16 v2, v88, v6, v2
	v_pk_fma_f16 v3, v89, v7, v3
	v_pk_fma_f16 v4, v90, v8, v4
	v_pk_fma_f16 v5, v91, v9, v5
	v_cndmask_b32_e64 v27, v27, v23, s[64:65]
	v_pk_fma_f16 v6, v2, v142, v143 op_sel:[0,0,0] op_sel_hi:[1,0,0] neg_lo:[1,0,0] neg_hi:[1,0,0]
	v_pk_fma_f16 v7, v3, v142, v143 op_sel:[0,0,0] op_sel_hi:[1,0,0] neg_lo:[1,0,0] neg_hi:[1,0,0]
	v_pk_fma_f16 v8, v4, v142, v143 op_sel:[0,0,0] op_sel_hi:[1,0,0] neg_lo:[1,0,0] neg_hi:[1,0,0]
	v_pk_fma_f16 v9, v5, v142, v143 op_sel:[0,0,0] op_sel_hi:[1,0,0] neg_lo:[1,0,0] neg_hi:[1,0,0]
	v_mfma_f32_16x16x32_f16 v[22:25], v[10:13], v[2:5], 0
	ds_read2_b64 v[52:55], v32 offset0:17 offset1:219
	v_pk_fma_f16 v2, v92, v6, v2
	v_pk_fma_f16 v3, v93, v7, v3
	v_pk_fma_f16 v4, v94, v8, v4
	v_pk_fma_f16 v5, v95, v9, v5
	v_cndmask_b32_e64 v28, v28, v20, s[64:65]
	s_waitcnt lgkmcnt(7)
	v_pk_fma_f16 v6, v2, v144, v145 op_sel:[0,0,0] op_sel_hi:[1,0,0] neg_lo:[1,0,0] neg_hi:[1,0,0]
	v_pk_fma_f16 v7, v3, v144, v145 op_sel:[0,0,0] op_sel_hi:[1,0,0] neg_lo:[1,0,0] neg_hi:[1,0,0]
	v_pk_fma_f16 v8, v4, v144, v145 op_sel:[0,0,0] op_sel_hi:[1,0,0] neg_lo:[1,0,0] neg_hi:[1,0,0]
	v_pk_fma_f16 v9, v5, v144, v145 op_sel:[0,0,0] op_sel_hi:[1,0,0] neg_lo:[1,0,0] neg_hi:[1,0,0]
	v_mfma_f32_16x16x32_f16 v[18:21], v[10:13], v[2:5], 0
	ds_read2_b64 v[56:59], v32 offset0:18 offset1:220
	ds_read_b128 v[124:127], v33 offset:144
	v_pk_fma_f16 v2, v96, v6, v2
	v_pk_fma_f16 v3, v97, v7, v3
	v_pk_fma_f16 v4, v98, v8, v4
	v_pk_fma_f16 v5, v99, v9, v5
	v_cndmask_b32_e64 v29, v29, v25, s[64:65]
	s_cmp_eq_u32 s72, 1
	s_cbranch_scc0 .Lc0_ns0
	s_waitcnt lgkmcnt(7)
	v_readfirstlane_b32 s4, v45
	s_cmp_eq_u32 s4, 4
	s_cbranch_scc0 .Lc0_dslow0
.Lc0_dback0:
	v_pk_add_f16 v112, v112, v116
	v_pk_add_f16 v113, v113, v117
	v_pk_add_f16 v114, v114, v118
	v_pk_add_f16 v115, v115, v119
	global_store_dwordx4 v35, v[112:115], s[68:69] offset:-1024 sc0 sc1
.Lc0_ns0:
	v_pk_fma_f16 v6, v2, v146, v147 op_sel:[0,0,0] op_sel_hi:[1,0,0] neg_lo:[1,0,0] neg_hi:[1,0,0]
	v_pk_fma_f16 v7, v3, v146, v147 op_sel:[0,0,0] op_sel_hi:[1,0,0] neg_lo:[1,0,0] neg_hi:[1,0,0]
	v_pk_fma_f16 v8, v4, v146, v147 op_sel:[0,0,0] op_sel_hi:[1,0,0] neg_lo:[1,0,0] neg_hi:[1,0,0]
	v_pk_fma_f16 v9, v5, v146, v147 op_sel:[0,0,0] op_sel_hi:[1,0,0] neg_lo:[1,0,0] neg_hi:[1,0,0]
	v_mfma_f32_16x16x32_f16 v[22:25], v[10:13], v[2:5], 0
	ds_read2_b64 v[60:63], v32 offset0:19 offset1:221
	v_pk_fma_f16 v2, v100, v6, v2
	v_pk_fma_f16 v3, v101, v7, v3
	v_pk_fma_f16 v4, v102, v8, v4
	v_pk_fma_f16 v5, v103, v9, v5
	v_cndmask_b32_e64 v26, v26, v18, s[66:67]
	s_waitcnt lgkmcnt(7)
	v_pk_fma_f16 v6, v2, v148, v149 op_sel:[0,0,0] op_sel_hi:[1,0,0] neg_lo:[1,0,0] neg_hi:[1,0,0]
	v_pk_fma_f16 v7, v3, v148, v149 op_sel:[0,0,0] op_sel_hi:[1,0,0] neg_lo:[1,0,0] neg_hi:[1,0,0]
	v_pk_fma_f16 v8, v4, v148, v149 op_sel:[0,0,0] op_sel_hi:[1,0,0] neg_lo:[1,0,0] neg_hi:[1,0,0]
	v_pk_fma_f16 v9, v5, v148, v149 op_sel:[0,0,0] op_sel_hi:[1,0,0] neg_lo:[1,0,0] neg_hi:[1,0,0]
	v_mfma_f32_16x16x32_f16 v[18:21], v[10:13], v[2:5], 0
	ds_read2_b64 v[64:67], v32 offset0:20 offset1:222
	ds_read_b128 v[128:131], v33 offset:160
	v_pk_fma_f16 v2, v104, v6, v2
	v_pk_fma_f16 v3, v105, v7, v3
	v_pk_fma_f16 v4, v106, v8, v4
	v_pk_fma_f16 v5, v107, v9, v5
	v_cndmask_b32_e64 v27, v27, v23, s[66:67]
	v_pk_fma_f16 v6, v2, v150, v151 op_sel:[0,0,0] op_sel_hi:[1,0,0] neg_lo:[1,0,0] neg_hi:[1,0,0]
	v_pk_fma_f16 v7, v3, v150, v151 op_sel:[0,0,0] op_sel_hi:[1,0,0] neg_lo:[1,0,0] neg_hi:[1,0,0]
	v_pk_fma_f16 v8, v4, v150, v151 op_sel:[0,0,0] op_sel_hi:[1,0,0] neg_lo:[1,0,0] neg_hi:[1,0,0]
	v_pk_fma_f16 v9, v5, v150, v151 op_sel:[0,0,0] op_sel_hi:[1,0,0] neg_lo:[1,0,0] neg_hi:[1,0,0]
	v_mfma_f32_16x16x32_f16 v[22:25], v[10:13], v[2:5], 0
	ds_read2_b64 v[68:71], v32 offset0:21 offset1:223
	v_pk_fma_f16 v2, v108, v6, v2
	v_pk_fma_f16 v3, v109, v7, v3
	v_pk_fma_f16 v4, v110, v8, v4
	v_pk_fma_f16 v5, v111, v9, v5
	v_cndmask_b32_e64 v28, v28, v20, s[66:67]
	s_waitcnt lgkmcnt(6)
	v_pk_fma_f16 v6, v2, v120, v121 op_sel:[0,0,0] op_sel_hi:[1,0,0] neg_lo:[1,0,0] neg_hi:[1,0,0]
	v_pk_fma_f16 v7, v3, v120, v121 op_sel:[0,0,0] op_sel_hi:[1,0,0] neg_lo:[1,0,0] neg_hi:[1,0,0]
	v_pk_fma_f16 v8, v4, v120, v121 op_sel:[0,0,0] op_sel_hi:[1,0,0] neg_lo:[1,0,0] neg_hi:[1,0,0]
	v_pk_fma_f16 v9, v5, v120, v121 op_sel:[0,0,0] op_sel_hi:[1,0,0] neg_lo:[1,0,0] neg_hi:[1,0,0]
	v_mfma_f32_16x16x32_f16 v[18:21], v[14:17], v[2:5], 0
	ds_read2_b64 v[72:75], v32 offset0:22 offset1:224
	ds_read_b128 v[132:135], v33 offset:176
	ds_read_b32 v37, v36 offset:8
	ds_read_b32 v38, v36 offset:72
	v_pk_fma_f16 v2, v48, v6, v2
	v_pk_fma_f16 v3, v49, v7, v3
	v_pk_fma_f16 v4, v50, v8, v4
	v_pk_fma_f16 v5, v51, v9, v5
	v_cndmask_b32_e64 v29, v29, v25, s[66:67]
	v_cvt_pk_f16_f32 v30, v26, v27
	v_cvt_pk_f16_f32 v31, v28, v29
	ds_write_b16 v39, v30 offset:2048
	ds_write_b16_d16_hi v39, v30 offset:2112
	ds_write_b16 v39, v31 offset:2176
	ds_write_b16_d16_hi v39, v31 offset:2240
	s_mov_b64 exec, 1
	ds_add_u32 v36, v44 offset:128
	s_mov_b64 exec, -1
	v_pk_fma_f16 v6, v2, v122, v123 op_sel:[0,0,0] op_sel_hi:[1,0,0] neg_lo:[1,0,0] neg_hi:[1,0,0]
	v_pk_fma_f16 v7, v3, v122, v123 op_sel:[0,0,0] op_sel_hi:[1,0,0] neg_lo:[1,0,0] neg_hi:[1,0,0]
	v_pk_fma_f16 v8, v4, v122, v123 op_sel:[0,0,0] op_sel_hi:[1,0,0] neg_lo:[1,0,0] neg_hi:[1,0,0]
	v_pk_fma_f16 v9, v5, v122, v123 op_sel:[0,0,0] op_sel_hi:[1,0,0] neg_lo:[1,0,0] neg_hi:[1,0,0]
	v_mfma_f32_16x16x32_f16 v[22:25], v[14:17], v[2:5], 0
	ds_read2_b64 v[76:79], v32 offset0:23 offset1:225
	v_pk_fma_f16 v2, v52, v6, v2
	v_pk_fma_f16 v3, v53, v7, v3
	v_pk_fma_f16 v4, v54, v8, v4
	v_pk_fma_f16 v5, v55, v9, v5
	v_cndmask_b32_e64 v26, v26, v18, s[60:61]
	s_waitcnt lgkmcnt(13)
	v_pk_fma_f16 v6, v2, v124, v125 op_sel:[0,0,0] op_sel_hi:[1,0,0] neg_lo:[1,0,0] neg_hi:[1,0,0]
	v_pk_fma_f16 v7, v3, v124, v125 op_sel:[0,0,0] op_sel_hi:[1,0,0] neg_lo:[1,0,0] neg_hi:[1,0,0]
	v_pk_fma_f16 v8, v4, v124, v125 op_sel:[0,0,0] op_sel_hi:[1,0,0] neg_lo:[1,0,0] neg_hi:[1,0,0]
	v_pk_fma_f16 v9, v5, v124, v125 op_sel:[0,0,0] op_sel_hi:[1,0,0] neg_lo:[1,0,0] neg_hi:[1,0,0]
	v_mfma_f32_16x16x32_f16 v[18:21], v[14:17], v[2:5], 0
	ds_read2_b64 v[80:83], v32 offset0:24 offset1:226
	ds_read_b128 v[136:139], v33 offset:192
	v_pk_fma_f16 v2, v56, v6, v2
	v_pk_fma_f16 v3, v57, v7, v3
	v_pk_fma_f16 v4, v58, v8, v4
	v_pk_fma_f16 v5, v59, v9, v5
	v_cndmask_b32_e64 v27, v27, v23, s[60:61]
	v_pk_fma_f16 v6, v2, v126, v127 op_sel:[0,0,0] op_sel_hi:[1,0,0] neg_lo:[1,0,0] neg_hi:[1,0,0]
	v_pk_fma_f16 v7, v3, v126, v127 op_sel:[0,0,0] op_sel_hi:[1,0,0] neg_lo:[1,0,0] neg_hi:[1,0,0]
	v_pk_fma_f16 v8, v4, v126, v127 op_sel:[0,0,0] op_sel_hi:[1,0,0] neg_lo:[1,0,0] neg_hi:[1,0,0]
	v_pk_fma_f16 v9, v5, v126, v127 op_sel:[0,0,0] op_sel_hi:[1,0,0] neg_lo:[1,0,0] neg_hi:[1,0,0]
	v_mfma_f32_16x16x32_f16 v[22:25], v[14:17], v[2:5], 0
	ds_read2_b64 v[84:87], v32 offset0:25 offset1:227
	v_pk_fma_f16 v2, v60, v6, v2
	v_pk_fma_f16 v3, v61, v7, v3
	v_pk_fma_f16 v4, v62, v8, v4
	v_pk_fma_f16 v5, v63, v9, v5
	v_cndmask_b32_e64 v28, v28, v20, s[60:61]
	s_waitcnt lgkmcnt(13)
	v_pk_fma_f16 v6, v2, v128, v129 op_sel:[0,0,0] op_sel_hi:[1,0,0] neg_lo:[1,0,0] neg_hi:[1,0,0]
	v_pk_fma_f16 v7, v3, v128, v129 op_sel:[0,0,0] op_sel_hi:[1,0,0] neg_lo:[1,0,0] neg_hi:[1,0,0]
	v_pk_fma_f16 v8, v4, v128, v129 op_sel:[0,0,0] op_sel_hi:[1,0,0] neg_lo:[1,0,0] neg_hi:[1,0,0]
	v_pk_fma_f16 v9, v5, v128, v129 op_sel:[0,0,0] op_sel_hi:[1,0,0] neg_lo:[1,0,0] neg_hi:[1,0,0]
	v_mfma_f32_16x16x32_f16 v[18:21], v[14:17], v[2:5], 0
	ds_read2_b64 v[88:91], v32 offset0:26 offset1:228
	ds_read_b128 v[140:143], v33 offset:208
	v_pk_fma_f16 v2, v64, v6, v2
	v_pk_fma_f16 v3, v65, v7, v3
	v_pk_fma_f16 v4, v66, v8, v4
	v_pk_fma_f16 v5, v67, v9, v5
	v_cndmask_b32_e64 v29, v29, v25, s[60:61]
	v_pk_fma_f16 v6, v2, v130, v131 op_sel:[0,0,0] op_sel_hi:[1,0,0] neg_lo:[1,0,0] neg_hi:[1,0,0]
	v_pk_fma_f16 v7, v3, v130, v131 op_sel:[0,0,0] op_sel_hi:[1,0,0] neg_lo:[1,0,0] neg_hi:[1,0,0]
	v_pk_fma_f16 v8, v4, v130, v131 op_sel:[0,0,0] op_sel_hi:[1,0,0] neg_lo:[1,0,0] neg_hi:[1,0,0]
	v_pk_fma_f16 v9, v5, v130, v131 op_sel:[0,0,0] op_sel_hi:[1,0,0] neg_lo:[1,0,0] neg_hi:[1,0,0]
	v_mfma_f32_16x16x32_f16 v[22:25], v[14:17], v[2:5], 0
	ds_read2_b64 v[92:95], v32 offset0:27 offset1:229
	v_pk_fma_f16 v2, v68, v6, v2
	v_pk_fma_f16 v3, v69, v7, v3
	v_pk_fma_f16 v4, v70, v8, v4
	v_pk_fma_f16 v5, v71, v9, v5
	v_cndmask_b32_e64 v26, v26, v18, s[62:63]
	s_waitcnt lgkmcnt(6)
	v_pk_fma_f16 v6, v2, v132, v133 op_sel:[0,0,0] op_sel_hi:[1,0,0] neg_lo:[1,0,0] neg_hi:[1,0,0]
	v_pk_fma_f16 v7, v3, v132, v133 op_sel:[0,0,0] op_sel_hi:[1,0,0] neg_lo:[1,0,0] neg_hi:[1,0,0]
	v_pk_fma_f16 v8, v4, v132, v133 op_sel:[0,0,0] op_sel_hi:[1,0,0] neg_lo:[1,0,0] neg_hi:[1,0,0]
	v_pk_fma_f16 v9, v5, v132, v133 op_sel:[0,0,0] op_sel_hi:[1,0,0] neg_lo:[1,0,0] neg_hi:[1,0,0]
	v_mfma_f32_16x16x32_f16 v[18:21], v[14:17], v[2:5], 0
	ds_read2_b64 v[96:99], v32 offset0:28 offset1:230
	ds_read_b128 v[144:147], v33 offset:224
	v_pk_fma_f16 v2, v72, v6, v2
	v_pk_fma_f16 v3, v73, v7, v3
	v_pk_fma_f16 v4, v74, v8, v4
	v_pk_fma_f16 v5, v75, v9, v5
	v_cndmask_b32_e64 v27, v27, v23, s[62:63]
	v_pk_fma_f16 v6, v2, v134, v135 op_sel:[0,0,0] op_sel_hi:[1,0,0] neg_lo:[1,0,0] neg_hi:[1,0,0]
	v_pk_fma_f16 v7, v3, v134, v135 op_sel:[0,0,0] op_sel_hi:[1,0,0] neg_lo:[1,0,0] neg_hi:[1,0,0]
	v_pk_fma_f16 v8, v4, v134, v135 op_sel:[0,0,0] op_sel_hi:[1,0,0] neg_lo:[1,0,0] neg_hi:[1,0,0]
	v_pk_fma_f16 v9, v5, v134, v135 op_sel:[0,0,0] op_sel_hi:[1,0,0] neg_lo:[1,0,0] neg_hi:[1,0,0]
	v_mfma_f32_16x16x32_f16 v[22:25], v[14:17], v[2:5], 0
	ds_read2_b64 v[100:103], v32 offset0:29 offset1:231
	v_pk_fma_f16 v2, v76, v6, v2
	v_pk_fma_f16 v3, v77, v7, v3
	v_pk_fma_f16 v4, v78, v8, v4
	v_pk_fma_f16 v5, v79, v9, v5
	v_cndmask_b32_e64 v28, v28, v20, s[62:63]
	s_waitcnt lgkmcnt(6)
	v_pk_fma_f16 v6, v2, v136, v137 op_sel:[0,0,0] op_sel_hi:[1,0,0] neg_lo:[1,0,0] neg_hi:[1,0,0]
	v_pk_fma_f16 v7, v3, v136, v137 op_sel:[0,0,0] op_sel_hi:[1,0,0] neg_lo:[1,0,0] neg_hi:[1,0,0]
	v_pk_fma_f16 v8, v4, v136, v137 op_sel:[0,0,0] op_sel_hi:[1,0,0] neg_lo:[1,0,0] neg_hi:[1,0,0]
	v_pk_fma_f16 v9, v5, v136, v137 op_sel:[0,0,0] op_sel_hi:[1,0,0] neg_lo:[1,0,0] neg_hi:[1,0,0]
	v_mfma_f32_16x16x32_f16 v[18:21], v[14:17], v[2:5], 0
	ds_read2_b64 v[104:107], v32 offset0:30 offset1:232
	ds_read_b128 v[148:151], v33 offset:240
	v_pk_fma_f16 v2, v80, v6, v2
	v_pk_fma_f16 v3, v81, v7, v3
	v_pk_fma_f16 v4, v82, v8, v4
	v_pk_fma_f16 v5, v83, v9, v5
	v_cndmask_b32_e64 v29, v29, v25, s[62:63]
	v_readfirstlane_b32 s4, v37
	v_readfirstlane_b32 s5, v38
	s_and_b32 s4, s4, s5
	s_cbranch_scc0 .Lc0_slow1
.Lc0_back1:
	s_mov_b32 s72, 0
	s_cmp_eq_u32 s36, s71
	s_cbranch_scc0 .Lc0_nd1
	s_mov_b32 s72, 1
	ds_read_b32 v45, v36 offset:128
	ds_read_b128 v[112:115], v43 offset:2048
	ds_read_b128 v[116:119], v43 offset:3072
.Lc0_nd1:
	v_pk_fma_f16 v6, v2, v138, v139 op_sel:[0,0,0] op_sel_hi:[1,0,0] neg_lo:[1,0,0] neg_hi:[1,0,0]
	v_pk_fma_f16 v7, v3, v138, v139 op_sel:[0,0,0] op_sel_hi:[1,0,0] neg_lo:[1,0,0] neg_hi:[1,0,0]
	v_pk_fma_f16 v8, v4, v138, v139 op_sel:[0,0,0] op_sel_hi:[1,0,0] neg_lo:[1,0,0] neg_hi:[1,0,0]
	v_pk_fma_f16 v9, v5, v138, v139 op_sel:[0,0,0] op_sel_hi:[1,0,0] neg_lo:[1,0,0] neg_hi:[1,0,0]
	v_mfma_f32_16x16x32_f16 v[22:25], v[14:17], v[2:5], 0
	ds_read2_b64 v[108:111], v32 offset0:31 offset1:233
	v_pk_fma_f16 v2, v84, v6, v2
	v_pk_fma_f16 v3, v85, v7, v3
	v_pk_fma_f16 v4, v86, v8, v4
	v_pk_fma_f16 v5, v87, v9, v5
	v_cndmask_b32_e64 v26, v26, v18, s[64:65]
	s_waitcnt lgkmcnt(6)
	v_pk_fma_f16 v6, v2, v140, v141 op_sel:[0,0,0] op_sel_hi:[1,0,0] neg_lo:[1,0,0] neg_hi:[1,0,0]
	v_pk_fma_f16 v7, v3, v140, v141 op_sel:[0,0,0] op_sel_hi:[1,0,0] neg_lo:[1,0,0] neg_hi:[1,0,0]
	v_pk_fma_f16 v8, v4, v140, v141 op_sel:[0,0,0] op_sel_hi:[1,0,0] neg_lo:[1,0,0] neg_hi:[1,0,0]
	v_pk_fma_f16 v9, v5, v140, v141 op_sel:[0,0,0] op_sel_hi:[1,0,0] neg_lo:[1,0,0] neg_hi:[1,0,0]
	v_mfma_f32_16x16x32_f16 v[18:21], v[14:17], v[2:5], 0
	ds_read2_b64 v[48:51], v32 offset0:32 offset1:234
	ds_read_b128 v[120:123], v33 offset:256
	ds_read2_b64 v[10:13], v34 offset0:32 offset1:234
	v_pk_fma_f16 v2, v88, v6, v2
	v_pk_fma_f16 v3, v89, v7, v3
	v_pk_fma_f16 v4, v90, v8, v4
	v_pk_fma_f16 v5, v91, v9, v5
	v_cndmask_b32_e64 v27, v27, v23, s[64:65]
	v_pk_fma_f16 v6, v2, v142, v143 op_sel:[0,0,0] op_sel_hi:[1,0,0] neg_lo:[1,0,0] neg_hi:[1,0,0]
	v_pk_fma_f16 v7, v3, v142, v143 op_sel:[0,0,0] op_sel_hi:[1,0,0] neg_lo:[1,0,0] neg_hi:[1,0,0]
	v_pk_fma_f16 v8, v4, v142, v143 op_sel:[0,0,0] op_sel_hi:[1,0,0] neg_lo:[1,0,0] neg_hi:[1,0,0]
	v_pk_fma_f16 v9, v5, v142, v143 op_sel:[0,0,0] op_sel_hi:[1,0,0] neg_lo:[1,0,0] neg_hi:[1,0,0]
	v_mfma_f32_16x16x32_f16 v[22:25], v[14:17], v[2:5], 0
	ds_read2_b64 v[52:55], v32 offset0:33 offset1:235
	v_pk_fma_f16 v2, v92, v6, v2
	v_pk_fma_f16 v3, v93, v7, v3
	v_pk_fma_f16 v4, v94, v8, v4
	v_pk_fma_f16 v5, v95, v9, v5
	v_cndmask_b32_e64 v28, v28, v20, s[64:65]
	s_waitcnt lgkmcnt(7)
	v_pk_fma_f16 v6, v2, v144, v145 op_sel:[0,0,0] op_sel_hi:[1,0,0] neg_lo:[1,0,0] neg_hi:[1,0,0]
	v_pk_fma_f16 v7, v3, v144, v145 op_sel:[0,0,0] op_sel_hi:[1,0,0] neg_lo:[1,0,0] neg_hi:[1,0,0]
	v_pk_fma_f16 v8, v4, v144, v145 op_sel:[0,0,0] op_sel_hi:[1,0,0] neg_lo:[1,0,0] neg_hi:[1,0,0]
	v_pk_fma_f16 v9, v5, v144, v145 op_sel:[0,0,0] op_sel_hi:[1,0,0] neg_lo:[1,0,0] neg_hi:[1,0,0]
	v_mfma_f32_16x16x32_f16 v[18:21], v[14:17], v[2:5], 0
	ds_read2_b64 v[56:59], v32 offset0:34 offset1:236
	ds_read_b128 v[124:127], v33 offset:272
	v_pk_fma_f16 v2, v96, v6, v2
	v_pk_fma_f16 v3, v97, v7, v3
	v_pk_fma_f16 v4, v98, v8, v4
	v_pk_fma_f16 v5, v99, v9, v5
	v_cndmask_b32_e64 v29, v29, v25, s[64:65]
	s_cmp_eq_u32 s72, 1
	s_cbranch_scc0 .Lc0_ns1
	s_waitcnt lgkmcnt(7)
	v_readfirstlane_b32 s4, v45
	s_cmp_eq_u32 s4, 4
	s_cbranch_scc0 .Lc0_dslow1
.Lc0_dback1:
	v_pk_add_f16 v112, v112, v116
	v_pk_add_f16 v113, v113, v117
	v_pk_add_f16 v114, v114, v118
	v_pk_add_f16 v115, v115, v119
	global_store_dwordx4 v35, v[112:115], s[68:69] offset:0 sc0 sc1
.Lc0_ns1:
	v_pk_fma_f16 v6, v2, v146, v147 op_sel:[0,0,0] op_sel_hi:[1,0,0] neg_lo:[1,0,0] neg_hi:[1,0,0]
	v_pk_fma_f16 v7, v3, v146, v147 op_sel:[0,0,0] op_sel_hi:[1,0,0] neg_lo:[1,0,0] neg_hi:[1,0,0]
	v_pk_fma_f16 v8, v4, v146, v147 op_sel:[0,0,0] op_sel_hi:[1,0,0] neg_lo:[1,0,0] neg_hi:[1,0,0]
	v_pk_fma_f16 v9, v5, v146, v147 op_sel:[0,0,0] op_sel_hi:[1,0,0] neg_lo:[1,0,0] neg_hi:[1,0,0]
	v_mfma_f32_16x16x32_f16 v[22:25], v[14:17], v[2:5], 0
	ds_read2_b64 v[60:63], v32 offset0:35 offset1:237
	v_pk_fma_f16 v2, v100, v6, v2
	v_pk_fma_f16 v3, v101, v7, v3
	v_pk_fma_f16 v4, v102, v8, v4
	v_pk_fma_f16 v5, v103, v9, v5
	v_cndmask_b32_e64 v26, v26, v18, s[66:67]
	s_waitcnt lgkmcnt(7)
	v_pk_fma_f16 v6, v2, v148, v149 op_sel:[0,0,0] op_sel_hi:[1,0,0] neg_lo:[1,0,0] neg_hi:[1,0,0]
	v_pk_fma_f16 v7, v3, v148, v149 op_sel:[0,0,0] op_sel_hi:[1,0,0] neg_lo:[1,0,0] neg_hi:[1,0,0]
	v_pk_fma_f16 v8, v4, v148, v149 op_sel:[0,0,0] op_sel_hi:[1,0,0] neg_lo:[1,0,0] neg_hi:[1,0,0]
	v_pk_fma_f16 v9, v5, v148, v149 op_sel:[0,0,0] op_sel_hi:[1,0,0] neg_lo:[1,0,0] neg_hi:[1,0,0]
	v_mfma_f32_16x16x32_f16 v[18:21], v[14:17], v[2:5], 0
	ds_read2_b64 v[64:67], v32 offset0:36 offset1:238
	ds_read_b128 v[128:131], v33 offset:288
	v_pk_fma_f16 v2, v104, v6, v2
	v_pk_fma_f16 v3, v105, v7, v3
	v_pk_fma_f16 v4, v106, v8, v4
	v_pk_fma_f16 v5, v107, v9, v5
	v_cndmask_b32_e64 v27, v27, v23, s[66:67]
	v_pk_fma_f16 v6, v2, v150, v151 op_sel:[0,0,0] op_sel_hi:[1,0,0] neg_lo:[1,0,0] neg_hi:[1,0,0]
	v_pk_fma_f16 v7, v3, v150, v151 op_sel:[0,0,0] op_sel_hi:[1,0,0] neg_lo:[1,0,0] neg_hi:[1,0,0]
	v_pk_fma_f16 v8, v4, v150, v151 op_sel:[0,0,0] op_sel_hi:[1,0,0] neg_lo:[1,0,0] neg_hi:[1,0,0]
	v_pk_fma_f16 v9, v5, v150, v151 op_sel:[0,0,0] op_sel_hi:[1,0,0] neg_lo:[1,0,0] neg_hi:[1,0,0]
	v_mfma_f32_16x16x32_f16 v[22:25], v[14:17], v[2:5], 0
	ds_read2_b64 v[68:71], v32 offset0:37 offset1:239
	v_pk_fma_f16 v2, v108, v6, v2
	v_pk_fma_f16 v3, v109, v7, v3
	v_pk_fma_f16 v4, v110, v8, v4
	v_pk_fma_f16 v5, v111, v9, v5
	v_cndmask_b32_e64 v28, v28, v20, s[66:67]
	v_add_u32_e32 v32, 0x100, v32
	v_add_u32_e32 v33, 0x100, v33
	v_add_u32_e32 v34, 0x100, v34
	v_add_u32_e32 v36, 8, v36
	v_add_u32_e32 v39, 0x1000, v39
	v_add_u32_e32 v43, 0x1000, v43
	v_add_u32_e32 v35, 0x800, v35
	s_xor_b32 s71, s71, 2
	s_add_i32 s70, s70, 1
	s_cmp_lt_u32 s70, 6
	s_cbranch_scc1 .Lc0_loop
	s_waitcnt lgkmcnt(6)
	v_pk_fma_f16 v6, v2, v120, v121 op_sel:[0,0,0] op_sel_hi:[1,0,0] neg_lo:[1,0,0] neg_hi:[1,0,0]
	v_pk_fma_f16 v7, v3, v120, v121 op_sel:[0,0,0] op_sel_hi:[1,0,0] neg_lo:[1,0,0] neg_hi:[1,0,0]
	v_pk_fma_f16 v8, v4, v120, v121 op_sel:[0,0,0] op_sel_hi:[1,0,0] neg_lo:[1,0,0] neg_hi:[1,0,0]
	v_pk_fma_f16 v9, v5, v120, v121 op_sel:[0,0,0] op_sel_hi:[1,0,0] neg_lo:[1,0,0] neg_hi:[1,0,0]
	v_mfma_f32_16x16x32_f16 v[18:21], v[10:13], v[2:5], 0
	ds_read2_b64 v[72:75], v32 offset0:6 offset1:208
	ds_read_b128 v[132:135], v33 offset:48
	v_pk_fma_f16 v2, v48, v6, v2
	v_pk_fma_f16 v3, v49, v7, v3
	v_pk_fma_f16 v4, v50, v8, v4
	v_pk_fma_f16 v5, v51, v9, v5
	v_cndmask_b32_e64 v29, v29, v25, s[66:67]
	v_cvt_pk_f16_f32 v30, v26, v27
	v_cvt_pk_f16_f32 v31, v28, v29
	ds_write_b16 v39, v30 offset:0
	ds_write_b16_d16_hi v39, v30 offset:64
	ds_write_b16 v39, v31 offset:128
	ds_write_b16_d16_hi v39, v31 offset:192
	s_mov_b64 exec, 1
	ds_add_u32 v36, v44 offset:124
	s_mov_b64 exec, -1
	v_pk_fma_f16 v6, v2, v122, v123 op_sel:[0,0,0] op_sel_hi:[1,0,0] neg_lo:[1,0,0] neg_hi:[1,0,0]
	v_pk_fma_f16 v7, v3, v122, v123 op_sel:[0,0,0] op_sel_hi:[1,0,0] neg_lo:[1,0,0] neg_hi:[1,0,0]
	v_pk_fma_f16 v8, v4, v122, v123 op_sel:[0,0,0] op_sel_hi:[1,0,0] neg_lo:[1,0,0] neg_hi:[1,0,0]
	v_pk_fma_f16 v9, v5, v122, v123 op_sel:[0,0,0] op_sel_hi:[1,0,0] neg_lo:[1,0,0] neg_hi:[1,0,0]
	v_mfma_f32_16x16x32_f16 v[22:25], v[10:13], v[2:5], 0
	ds_read2_b64 v[76:79], v32 offset0:7 offset1:209
	v_pk_fma_f16 v2, v52, v6, v2
	v_pk_fma_f16 v3, v53, v7, v3
	v_pk_fma_f16 v4, v54, v8, v4
	v_pk_fma_f16 v5, v55, v9, v5
	v_cndmask_b32_e64 v26, v26, v18, s[60:61]
	s_waitcnt lgkmcnt(11)
	v_pk_fma_f16 v6, v2, v124, v125 op_sel:[0,0,0] op_sel_hi:[1,0,0] neg_lo:[1,0,0] neg_hi:[1,0,0]
	v_pk_fma_f16 v7, v3, v124, v125 op_sel:[0,0,0] op_sel_hi:[1,0,0] neg_lo:[1,0,0] neg_hi:[1,0,0]
	v_pk_fma_f16 v8, v4, v124, v125 op_sel:[0,0,0] op_sel_hi:[1,0,0] neg_lo:[1,0,0] neg_hi:[1,0,0]
	v_pk_fma_f16 v9, v5, v124, v125 op_sel:[0,0,0] op_sel_hi:[1,0,0] neg_lo:[1,0,0] neg_hi:[1,0,0]
	v_mfma_f32_16x16x32_f16 v[18:21], v[10:13], v[2:5], 0
	v_pk_fma_f16 v2, v56, v6, v2
	v_pk_fma_f16 v3, v57, v7, v3
	v_pk_fma_f16 v4, v58, v8, v4
	v_pk_fma_f16 v5, v59, v9, v5
	v_cndmask_b32_e64 v27, v27, v23, s[60:61]
	v_pk_fma_f16 v6, v2, v126, v127 op_sel:[0,0,0] op_sel_hi:[1,0,0] neg_lo:[1,0,0] neg_hi:[1,0,0]
	v_pk_fma_f16 v7, v3, v126, v127 op_sel:[0,0,0] op_sel_hi:[1,0,0] neg_lo:[1,0,0] neg_hi:[1,0,0]
	v_pk_fma_f16 v8, v4, v126, v127 op_sel:[0,0,0] op_sel_hi:[1,0,0] neg_lo:[1,0,0] neg_hi:[1,0,0]
	v_pk_fma_f16 v9, v5, v126, v127 op_sel:[0,0,0] op_sel_hi:[1,0,0] neg_lo:[1,0,0] neg_hi:[1,0,0]
	v_mfma_f32_16x16x32_f16 v[22:25], v[10:13], v[2:5], 0
	v_pk_fma_f16 v2, v60, v6, v2
	v_pk_fma_f16 v3, v61, v7, v3
	v_pk_fma_f16 v4, v62, v8, v4
	v_pk_fma_f16 v5, v63, v9, v5
	v_cndmask_b32_e64 v28, v28, v20, s[60:61]
	s_waitcnt lgkmcnt(8)
	s_mov_b32 s72, 0
	s_cmp_eq_u32 s70, 0
	s_cbranch_scc1 .Lc0_ndt
	s_sub_i32 s4, 3, s71
	s_cmp_eq_u32 s36, s4
	s_cbranch_scc0 .Lc0_ndt
	s_mov_b32 s72, 1
	ds_read_b32 v45, v36 offset:124
	ds_read_b128 v[112:115], v43 offset:0
	ds_read_b128 v[116:119], v43 offset:1024
.Lc0_ndt:
	v_pk_fma_f16 v6, v2, v128, v129 op_sel:[0,0,0] op_sel_hi:[1,0,0] neg_lo:[1,0,0] neg_hi:[1,0,0]
	v_pk_fma_f16 v7, v3, v128, v129 op_sel:[0,0,0] op_sel_hi:[1,0,0] neg_lo:[1,0,0] neg_hi:[1,0,0]
	v_pk_fma_f16 v8, v4, v128, v129 op_sel:[0,0,0] op_sel_hi:[1,0,0] neg_lo:[1,0,0] neg_hi:[1,0,0]
	v_pk_fma_f16 v9, v5, v128, v129 op_sel:[0,0,0] op_sel_hi:[1,0,0] neg_lo:[1,0,0] neg_hi:[1,0,0]
	v_mfma_f32_16x16x32_f16 v[18:21], v[10:13], v[2:5], 0
	v_pk_fma_f16 v2, v64, v6, v2
	v_pk_fma_f16 v3, v65, v7, v3
	v_pk_fma_f16 v4, v66, v8, v4
	v_pk_fma_f16 v5, v67, v9, v5
	v_cndmask_b32_e64 v29, v29, v25, s[60:61]
	v_pk_fma_f16 v6, v2, v130, v131 op_sel:[0,0,0] op_sel_hi:[1,0,0] neg_lo:[1,0,0] neg_hi:[1,0,0]
	v_pk_fma_f16 v7, v3, v130, v131 op_sel:[0,0,0] op_sel_hi:[1,0,0] neg_lo:[1,0,0] neg_hi:[1,0,0]
	v_pk_fma_f16 v8, v4, v130, v131 op_sel:[0,0,0] op_sel_hi:[1,0,0] neg_lo:[1,0,0] neg_hi:[1,0,0]
	v_pk_fma_f16 v9, v5, v130, v131 op_sel:[0,0,0] op_sel_hi:[1,0,0] neg_lo:[1,0,0] neg_hi:[1,0,0]
	v_mfma_f32_16x16x32_f16 v[22:25], v[10:13], v[2:5], 0
	v_pk_fma_f16 v2, v68, v6, v2
	v_pk_fma_f16 v3, v69, v7, v3
	v_pk_fma_f16 v4, v70, v8, v4
	v_pk_fma_f16 v5, v71, v9, v5
	v_cndmask_b32_e64 v26, v26, v18, s[62:63]
	s_waitcnt lgkmcnt(0)
	v_pk_fma_f16 v6, v2, v132, v133 op_sel:[0,0,0] op_sel_hi:[1,0,0] neg_lo:[1,0,0] neg_hi:[1,0,0]
	v_pk_fma_f16 v7, v3, v132, v133 op_sel:[0,0,0] op_sel_hi:[1,0,0] neg_lo:[1,0,0] neg_hi:[1,0,0]
	v_pk_fma_f16 v8, v4, v132, v133 op_sel:[0,0,0] op_sel_hi:[1,0,0] neg_lo:[1,0,0] neg_hi:[1,0,0]
	v_pk_fma_f16 v9, v5, v132, v133 op_sel:[0,0,0] op_sel_hi:[1,0,0] neg_lo:[1,0,0] neg_hi:[1,0,0]
	v_mfma_f32_16x16x32_f16 v[18:21], v[10:13], v[2:5], 0
	v_pk_fma_f16 v2, v72, v6, v2
	v_pk_fma_f16 v3, v73, v7, v3
	v_pk_fma_f16 v4, v74, v8, v4
	v_pk_fma_f16 v5, v75, v9, v5
	v_cndmask_b32_e64 v27, v27, v23, s[62:63]
	s_cmp_eq_u32 s72, 1
	s_cbranch_scc0 .Lc0_nst
	s_waitcnt lgkmcnt(0)
	v_readfirstlane_b32 s4, v45
	s_cmp_eq_u32 s4, 4
	s_cbranch_scc0 .Lc0_dslowt

.Lc0_nst:
	v_pk_fma_f16 v6, v2, v134, v135 op_sel:[0,0,0] op_sel_hi:[1,0,0] neg_lo:[1,0,0] neg_hi:[1,0,0]
	v_pk_fma_f16 v7, v3, v134, v135 op_sel:[0,0,0] op_sel_hi:[1,0,0] neg_lo:[1,0,0] neg_hi:[1,0,0]
	v_pk_fma_f16 v8, v4, v134, v135 op_sel:[0,0,0] op_sel_hi:[1,0,0] neg_lo:[1,0,0] neg_hi:[1,0,0]
	v_pk_fma_f16 v9, v5, v134, v135 op_sel:[0,0,0] op_sel_hi:[1,0,0] neg_lo:[1,0,0] neg_hi:[1,0,0]
	v_mfma_f32_16x16x32_f16 v[22:25], v[10:13], v[2:5], 0
	v_pk_fma_f16 v2, v76, v6, v2
	v_pk_fma_f16 v3, v77, v7, v3
	v_pk_fma_f16 v4, v78, v8, v4
	v_pk_fma_f16 v5, v79, v9, v5
	v_cndmask_b32_e64 v28, v28, v20, s[62:63]
	s_nop 7
	v_cndmask_b32_e64 v29, v29, v25, s[62:63]
	v_cvt_pk_f16_f32 v30, v26, v27
	v_cvt_pk_f16_f32 v31, v28, v29
	ds_write_b16 v39, v30 offset:2048
	ds_write_b16_d16_hi v39, v30 offset:2112
	ds_write_b16 v39, v31 offset:2176
	ds_write_b16_d16_hi v39, v31 offset:2240
	s_mov_b64 exec, 1
	ds_add_u32 v36, v44 offset:128
	s_mov_b64 exec, -1
	s_cmp_eq_u32 s36, 0
	s_cbranch_scc0 .Lc0_end
.Lc0_fin:
	ds_read_b32 v45, v36 offset:128
	s_waitcnt lgkmcnt(0)
	v_readfirstlane_b32 s4, v45
	s_cmp_eq_u32 s4, 4
	s_cbranch_scc1 .Lc0_fin2
	s_sleep 1
	s_add_i32 s73, s73, 1
	s_cmp_lt_u32 s73, 0x4000
	s_cbranch_scc1 .Lc0_fin
.Lc0_fin2:
	ds_read_b128 v[112:115], v43 offset:2048
	ds_read_b128 v[116:119], v43 offset:3072
	s_waitcnt lgkmcnt(0)
	v_pk_add_f16 v112, v112, v116
	v_pk_add_f16 v113, v113, v117
	v_pk_add_f16 v114, v114, v118
	v_pk_add_f16 v115, v115, v119
	s_mov_b32 exec_lo, -1
	s_mov_b32 exec_hi, 0
	global_store_dwordx4 v35, v[112:115], s[68:69] sc0 sc1

.Lc0_slow0:
	s_sleep 1
	ds_read_b32 v37, v36 offset:4
	ds_read_b32 v38, v36 offset:68
	s_waitcnt lgkmcnt(0)
	v_readfirstlane_b32 s4, v37
	v_readfirstlane_b32 s5, v38
	s_and_b32 s4, s4, s5
	s_cbranch_scc1 .Lc0_back0
	s_add_i32 s73, s73, 1
	s_cmp_lt_u32 s73, 0x4000
	s_cbranch_scc1 .Lc0_slow0
	s_branch .Lc0_back0
.Lc0_dslow0:
	s_sleep 1
	ds_read_b32 v45, v36 offset:124
	s_waitcnt lgkmcnt(0)
	v_readfirstlane_b32 s4, v45
	s_cmp_eq_u32 s4, 4
	s_cbranch_scc1 .Lc0_dgo0
	s_add_i32 s73, s73, 1
	s_cmp_lt_u32 s73, 0x4000
	s_cbranch_scc1 .Lc0_dslow0
.Lc0_dgo0:
	ds_read_b128 v[112:115], v43 offset:0
	ds_read_b128 v[116:119], v43 offset:1024
	s_waitcnt lgkmcnt(0)
	s_branch .Lc0_dback0
.Lc0_slow1:
	s_sleep 1
	ds_read_b32 v37, v36 offset:8
	ds_read_b32 v38, v36 offset:72
	s_waitcnt lgkmcnt(0)
	v_readfirstlane_b32 s4, v37
	v_readfirstlane_b32 s5, v38
	s_and_b32 s4, s4, s5
	s_cbranch_scc1 .Lc0_back1
	s_add_i32 s73, s73, 1
	s_cmp_lt_u32 s73, 0x4000
	s_cbranch_scc1 .Lc0_slow1
	s_branch .Lc0_back1
.Lc0_dslow1:
	s_sleep 1
	ds_read_b32 v45, v36 offset:128
	s_waitcnt lgkmcnt(0)
	v_readfirstlane_b32 s4, v45
	s_cmp_eq_u32 s4, 4
	s_cbranch_scc1 .Lc0_dgo1
	s_add_i32 s73, s73, 1
	s_cmp_lt_u32 s73, 0x4000
	s_cbranch_scc1 .Lc0_dslow1
.Lc0_dgo1:
	ds_read_b128 v[112:115], v43 offset:2048
	ds_read_b128 v[116:119], v43 offset:3072
	s_waitcnt lgkmcnt(0)
	s_branch .Lc0_dback1

.Lc_par1:
	ds_read2_b64 v[48:51], v32 offset0:0 offset1:202
	ds_read_b128 v[120:123], v33 offset:0
	ds_read2_b64 v[10:13], v34 offset0:0 offset1:202
	ds_read2_b64 v[52:55], v32 offset0:1 offset1:203
	ds_read2_b64 v[56:59], v32 offset0:2 offset1:204
	ds_read_b128 v[124:127], v33 offset:16
	ds_read2_b64 v[60:63], v32 offset0:3 offset1:205
	ds_read2_b64 v[64:67], v32 offset0:4 offset1:206
	ds_read_b128 v[128:131], v33 offset:32
	ds_read2_b64 v[68:71], v32 offset0:5 offset1:207
	s_mov_b32 s70, 0
	s_mov_b32 s71, 0
.Lc1_loop:
	s_waitcnt lgkmcnt(6)
	v_pk_fma_f16 v6, v2, v120, v121 op_sel:[0,1,1] op_sel_hi:[1,1,1] neg_lo:[1,0,0] neg_hi:[1,0,0]
	v_pk_fma_f16 v7, v3, v120, v121 op_sel:[0,1,1] op_sel_hi:[1,1,1] neg_lo:[1,0,0] neg_hi:[1,0,0]
	v_pk_fma_f16 v8, v4, v120, v121 op_sel:[0,1,1] op_sel_hi:[1,1,1] neg_lo:[1,0,0] neg_hi:[1,0,0]
	v_pk_fma_f16 v9, v5, v120, v121 op_sel:[0,1,1] op_sel_hi:[1,1,1] neg_lo:[1,0,0] neg_hi:[1,0,0]
	v_mfma_f32_16x16x32_f16 v[18:21], v[10:13], v[2:5], 0
	ds_read2_b64 v[72:75], v32 offset0:6 offset1:208
	ds_read_b128 v[132:135], v33 offset:48
	ds_read_b32 v37, v36 offset:4
	ds_read_b32 v38, v36 offset:68
	v_pk_fma_f16 v2, v48, v6, v2
	v_pk_fma_f16 v3, v49, v7, v3
	v_pk_fma_f16 v4, v50, v8, v4
	v_pk_fma_f16 v5, v51, v9, v5
	v_cndmask_b32_e64 v29, v29, v25, s[66:67]
	v_cvt_pk_f16_f32 v30, v26, v27
	v_cvt_pk_f16_f32 v31, v28, v29
	ds_write_b16 v39, v30 offset:0
	ds_write_b16_d16_hi v39, v30 offset:64
	ds_write_b16 v39, v31 offset:128
	ds_write_b16_d16_hi v39, v31 offset:192
	s_mov_b64 exec, 1
	ds_add_u32 v36, v44 offset:124
	s_mov_b64 exec, -1
	v_pk_fma_f16 v6, v2, v122, v123 op_sel:[0,1,1] op_sel_hi:[1,1,1] neg_lo:[1,0,0] neg_hi:[1,0,0]
	v_pk_fma_f16 v7, v3, v122, v123 op_sel:[0,1,1] op_sel_hi:[1,1,1] neg_lo:[1,0,0] neg_hi:[1,0,0]
	v_pk_fma_f16 v8, v4, v122, v123 op_sel:[0,1,1] op_sel_hi:[1,1,1] neg_lo:[1,0,0] neg_hi:[1,0,0]
	v_pk_fma_f16 v9, v5, v122, v123 op_sel:[0,1,1] op_sel_hi:[1,1,1] neg_lo:[1,0,0] neg_hi:[1,0,0]
	v_mfma_f32_16x16x32_f16 v[22:25], v[10:13], v[2:5], 0
	ds_read2_b64 v[76:79], v32 offset0:7 offset1:209
	v_pk_fma_f16 v2, v52, v6, v2
	v_pk_fma_f16 v3, v53, v7, v3
	v_pk_fma_f16 v4, v54, v8, v4
	v_pk_fma_f16 v5, v55, v9, v5
	v_cndmask_b32_e64 v26, v26, v18, s[60:61]
	s_waitcnt lgkmcnt(13)
	v_pk_fma_f16 v6, v2, v124, v125 op_sel:[0,1,1] op_sel_hi:[1,1,1] neg_lo:[1,0,0] neg_hi:[1,0,0]
	v_pk_fma_f16 v7, v3, v124, v125 op_sel:[0,1,1] op_sel_hi:[1,1,1] neg_lo:[1,0,0] neg_hi:[1,0,0]
	v_pk_fma_f16 v8, v4, v124, v125 op_sel:[0,1,1] op_sel_hi:[1,1,1] neg_lo:[1,0,0] neg_hi:[1,0,0]
	v_pk_fma_f16 v9, v5, v124, v125 op_sel:[0,1,1] op_sel_hi:[1,1,1] neg_lo:[1,0,0] neg_hi:[1,0,0]
	v_mfma_f32_16x16x32_f16 v[18:21], v[10:13], v[2:5], 0
	ds_read2_b64 v[80:83], v32 offset0:8 offset1:210
	ds_read_b128 v[136:139], v33 offset:64
	v_pk_fma_f16 v2, v56, v6, v2
	v_pk_fma_f16 v3, v57, v7, v3
	v_pk_fma_f16 v4, v58, v8, v4
	v_pk_fma_f16 v5, v59, v9, v5
	v_cndmask_b32_e64 v27, v27, v23, s[60:61]
	v_pk_fma_f16 v6, v2, v126, v127 op_sel:[0,1,1] op_sel_hi:[1,1,1] neg_lo:[1,0,0] neg_hi:[1,0,0]
	v_pk_fma_f16 v7, v3, v126, v127 op_sel:[0,1,1] op_sel_hi:[1,1,1] neg_lo:[1,0,0] neg_hi:[1,0,0]
	v_pk_fma_f16 v8, v4, v126, v127 op_sel:[0,1,1] op_sel_hi:[1,1,1] neg_lo:[1,0,0] neg_hi:[1,0,0]
	v_pk_fma_f16 v9, v5, v126, v127 op_sel:[0,1,1] op_sel_hi:[1,1,1] neg_lo:[1,0,0] neg_hi:[1,0,0]
	v_mfma_f32_16x16x32_f16 v[22:25], v[10:13], v[2:5], 0
	ds_read2_b64 v[84:87], v32 offset0:9 offset1:211
	v_pk_fma_f16 v2, v60, v6, v2
	v_pk_fma_f16 v3, v61, v7, v3
	v_pk_fma_f16 v4, v62, v8, v4
	v_pk_fma_f16 v5, v63, v9, v5
	v_cndmask_b32_e64 v28, v28, v20, s[60:61]
	s_waitcnt lgkmcnt(13)
	v_pk_fma_f16 v6, v2, v128, v129 op_sel:[0,1,1] op_sel_hi:[1,1,1] neg_lo:[1,0,0] neg_hi:[1,0,0]
	v_pk_fma_f16 v7, v3, v128, v129 op_sel:[0,1,1] op_sel_hi:[1,1,1] neg_lo:[1,0,0] neg_hi:[1,0,0]
	v_pk_fma_f16 v8, v4, v128, v129 op_sel:[0,1,1] op_sel_hi:[1,1,1] neg_lo:[1,0,0] neg_hi:[1,0,0]
	v_pk_fma_f16 v9, v5, v128, v129 op_sel:[0,1,1] op_sel_hi:[1,1,1] neg_lo:[1,0,0] neg_hi:[1,0,0]
	v_mfma_f32_16x16x32_f16 v[18:21], v[10:13], v[2:5], 0
	ds_read2_b64 v[88:91], v32 offset0:10 offset1:212
	ds_read_b128 v[140:143], v33 offset:80
	v_pk_fma_f16 v2, v64, v6, v2
	v_pk_fma_f16 v3, v65, v7, v3
	v_pk_fma_f16 v4, v66, v8, v4
	v_pk_fma_f16 v5, v67, v9, v5
	v_cndmask_b32_e64 v29, v29, v25, s[60:61]
	v_pk_fma_f16 v6, v2, v130, v131 op_sel:[0,1,1] op_sel_hi:[1,1,1] neg_lo:[1,0,0] neg_hi:[1,0,0]
	v_pk_fma_f16 v7, v3, v130, v131 op_sel:[0,1,1] op_sel_hi:[1,1,1] neg_lo:[1,0,0] neg_hi:[1,0,0]
	v_pk_fma_f16 v8, v4, v130, v131 op_sel:[0,1,1] op_sel_hi:[1,1,1] neg_lo:[1,0,0] neg_hi:[1,0,0]
	v_pk_fma_f16 v9, v5, v130, v131 op_sel:[0,1,1] op_sel_hi:[1,1,1] neg_lo:[1,0,0] neg_hi:[1,0,0]
	v_mfma_f32_16x16x32_f16 v[22:25], v[10:13], v[2:5], 0
	ds_read2_b64 v[92:95], v32 offset0:11 offset1:213
	v_pk_fma_f16 v2, v68, v6, v2
	v_pk_fma_f16 v3, v69, v7, v3
	v_pk_fma_f16 v4, v70, v8, v4
	v_pk_fma_f16 v5, v71, v9, v5
	v_cndmask_b32_e64 v26, v26, v18, s[62:63]
	s_waitcnt lgkmcnt(6)
	v_pk_fma_f16 v6, v2, v132, v133 op_sel:[0,1,1] op_sel_hi:[1,1,1] neg_lo:[1,0,0] neg_hi:[1,0,0]
	v_pk_fma_f16 v7, v3, v132, v133 op_sel:[0,1,1] op_sel_hi:[1,1,1] neg_lo:[1,0,0] neg_hi:[1,0,0]
	v_pk_fma_f16 v8, v4, v132, v133 op_sel:[0,1,1] op_sel_hi:[1,1,1] neg_lo:[1,0,0] neg_hi:[1,0,0]
	v_pk_fma_f16 v9, v5, v132, v133 op_sel:[0,1,1] op_sel_hi:[1,1,1] neg_lo:[1,0,0] neg_hi:[1,0,0]
	v_mfma_f32_16x16x32_f16 v[18:21], v[10:13], v[2:5], 0
	ds_read2_b64 v[96:99], v32 offset0:12 offset1:214
	ds_read_b128 v[144:147], v33 offset:96
	v_pk_fma_f16 v2, v72, v6, v2
	v_pk_fma_f16 v3, v73, v7, v3
	v_pk_fma_f16 v4, v74, v8, v4
	v_pk_fma_f16 v5, v75, v9, v5
	v_cndmask_b32_e64 v27, v27, v23, s[62:63]
	v_pk_fma_f16 v6, v2, v134, v135 op_sel:[0,1,1] op_sel_hi:[1,1,1] neg_lo:[1,0,0] neg_hi:[1,0,0]
	v_pk_fma_f16 v7, v3, v134, v135 op_sel:[0,1,1] op_sel_hi:[1,1,1] neg_lo:[1,0,0] neg_hi:[1,0,0]
	v_pk_fma_f16 v8, v4, v134, v135 op_sel:[0,1,1] op_sel_hi:[1,1,1] neg_lo:[1,0,0] neg_hi:[1,0,0]
	v_pk_fma_f16 v9, v5, v134, v135 op_sel:[0,1,1] op_sel_hi:[1,1,1] neg_lo:[1,0,0] neg_hi:[1,0,0]
	v_mfma_f32_16x16x32_f16 v[22:25], v[10:13], v[2:5], 0
	ds_read2_b64 v[100:103], v32 offset0:13 offset1:215
	v_pk_fma_f16 v2, v76, v6, v2
	v_pk_fma_f16 v3, v77, v7, v3
	v_pk_fma_f16 v4, v78, v8, v4
	v_pk_fma_f16 v5, v79, v9, v5
	v_cndmask_b32_e64 v28, v28, v20, s[62:63]
	s_waitcnt lgkmcnt(6)
	v_pk_fma_f16 v6, v2, v136, v137 op_sel:[0,1,1] op_sel_hi:[1,1,1] neg_lo:[1,0,0] neg_hi:[1,0,0]
	v_pk_fma_f16 v7, v3, v136, v137 op_sel:[0,1,1] op_sel_hi:[1,1,1] neg_lo:[1,0,0] neg_hi:[1,0,0]
	v_pk_fma_f16 v8, v4, v136, v137 op_sel:[0,1,1] op_sel_hi:[1,1,1] neg_lo:[1,0,0] neg_hi:[1,0,0]
	v_pk_fma_f16 v9, v5, v136, v137 op_sel:[0,1,1] op_sel_hi:[1,1,1] neg_lo:[1,0,0] neg_hi:[1,0,0]
	v_mfma_f32_16x16x32_f16 v[18:21], v[10:13], v[2:5], 0
	ds_read2_b64 v[104:107], v32 offset0:14 offset1:216
	ds_read_b128 v[148:151], v33 offset:112
	v_pk_fma_f16 v2, v80, v6, v2
	v_pk_fma_f16 v3, v81, v7, v3
	v_pk_fma_f16 v4, v82, v8, v4
	v_pk_fma_f16 v5, v83, v9, v5
	v_cndmask_b32_e64 v29, v29, v25, s[62:63]
	v_readfirstlane_b32 s4, v37
	v_readfirstlane_b32 s5, v38
	s_and_b32 s4, s4, s5
	s_cbranch_scc0 .Lc1_slow0

.Lc1_nd0:
	v_pk_fma_f16 v6, v2, v138, v139 op_sel:[0,1,1] op_sel_hi:[1,1,1] neg_lo:[1,0,0] neg_hi:[1,0,0]
	v_pk_fma_f16 v7, v3, v138, v139 op_sel:[0,1,1] op_sel_hi:[1,1,1] neg_lo:[1,0,0] neg_hi:[1,0,0]
	v_pk_fma_f16 v8, v4, v138, v139 op_sel:[0,1,1] op_sel_hi:[1,1,1] neg_lo:[1,0,0] neg_hi:[1,0,0]
	v_pk_fma_f16 v9, v5, v138, v139 op_sel:[0,1,1] op_sel_hi:[1,1,1] neg_lo:[1,0,0] neg_hi:[1,0,0]
	v_mfma_f32_16x16x32_f16 v[22:25], v[10:13], v[2:5], 0
	ds_read2_b64 v[108:111], v32 offset0:15 offset1:217
	v_pk_fma_f16 v2, v84, v6, v2
	v_pk_fma_f16 v3, v85, v7, v3
	v_pk_fma_f16 v4, v86, v8, v4
	v_pk_fma_f16 v5, v87, v9, v5
	v_cndmask_b32_e64 v26, v26, v18, s[64:65]
	s_waitcnt lgkmcnt(6)
	v_pk_fma_f16 v6, v2, v140, v141 op_sel:[0,1,1] op_sel_hi:[1,1,1] neg_lo:[1,0,0] neg_hi:[1,0,0]
	v_pk_fma_f16 v7, v3, v140, v141 op_sel:[0,1,1] op_sel_hi:[1,1,1] neg_lo:[1,0,0] neg_hi:[1,0,0]
	v_pk_fma_f16 v8, v4, v140, v141 op_sel:[0,1,1] op_sel_hi:[1,1,1] neg_lo:[1,0,0] neg_hi:[1,0,0]
	v_pk_fma_f16 v9, v5, v140, v141 op_sel:[0,1,1] op_sel_hi:[1,1,1] neg_lo:[1,0,0] neg_hi:[1,0,0]
	v_mfma_f32_16x16x32_f16 v[18:21], v[10:13], v[2:5], 0
	ds_read2_b64 v[48:51], v32 offset0:16 offset1:218
	ds_read_b128 v[120:123], v33 offset:128
	ds_read2_b64 v[14:17], v34 offset0:16 offset1:218
	v_pk_fma_f16 v2, v88, v6, v2
	v_pk_fma_f16 v3, v89, v7, v3
	v_pk_fma_f16 v4, v90, v8, v4
	v_pk_fma_f16 v5, v91, v9, v5
	v_cndmask_b32_e64 v27, v27, v23, s[64:65]
	v_pk_fma_f16 v6, v2, v142, v143 op_sel:[0,1,1] op_sel_hi:[1,1,1] neg_lo:[1,0,0] neg_hi:[1,0,0]
	v_pk_fma_f16 v7, v3, v142, v143 op_sel:[0,1,1] op_sel_hi:[1,1,1] neg_lo:[1,0,0] neg_hi:[1,0,0]
	v_pk_fma_f16 v8, v4, v142, v143 op_sel:[0,1,1] op_sel_hi:[1,1,1] neg_lo:[1,0,0] neg_hi:[1,0,0]
	v_pk_fma_f16 v9, v5, v142, v143 op_sel:[0,1,1] op_sel_hi:[1,1,1] neg_lo:[1,0,0] neg_hi:[1,0,0]
	v_mfma_f32_16x16x32_f16 v[22:25], v[10:13], v[2:5], 0
	ds_read2_b64 v[52:55], v32 offset0:17 offset1:219
	v_pk_fma_f16 v2, v92, v6, v2
	v_pk_fma_f16 v3, v93, v7, v3
	v_pk_fma_f16 v4, v94, v8, v4
	v_pk_fma_f16 v5, v95, v9, v5
	v_cndmask_b32_e64 v28, v28, v20, s[64:65]
	s_waitcnt lgkmcnt(7)
	v_pk_fma_f16 v6, v2, v144, v145 op_sel:[0,1,1] op_sel_hi:[1,1,1] neg_lo:[1,0,0] neg_hi:[1,0,0]
	v_pk_fma_f16 v7, v3, v144, v145 op_sel:[0,1,1] op_sel_hi:[1,1,1] neg_lo:[1,0,0] neg_hi:[1,0,0]
	v_pk_fma_f16 v8, v4, v144, v145 op_sel:[0,1,1] op_sel_hi:[1,1,1] neg_lo:[1,0,0] neg_hi:[1,0,0]
	v_pk_fma_f16 v9, v5, v144, v145 op_sel:[0,1,1] op_sel_hi:[1,1,1] neg_lo:[1,0,0] neg_hi:[1,0,0]
	v_mfma_f32_16x16x32_f16 v[18:21], v[10:13], v[2:5], 0
	ds_read2_b64 v[56:59], v32 offset0:18 offset1:220
	ds_read_b128 v[124:127], v33 offset:144
	v_pk_fma_f16 v2, v96, v6, v2
	v_pk_fma_f16 v3, v97, v7, v3
	v_pk_fma_f16 v4, v98, v8, v4
	v_pk_fma_f16 v5, v99, v9, v5
	v_cndmask_b32_e64 v29, v29, v25, s[64:65]
	s_cmp_eq_u32 s72, 1
	s_cbranch_scc0 .Lc1_ns0
	s_waitcnt lgkmcnt(7)
	v_readfirstlane_b32 s4, v45
	s_cmp_eq_u32 s4, 4
	s_cbranch_scc0 .Lc1_dslow0

.Lc1_ns0:
	v_pk_fma_f16 v6, v2, v146, v147 op_sel:[0,1,1] op_sel_hi:[1,1,1] neg_lo:[1,0,0] neg_hi:[1,0,0]
	v_pk_fma_f16 v7, v3, v146, v147 op_sel:[0,1,1] op_sel_hi:[1,1,1] neg_lo:[1,0,0] neg_hi:[1,0,0]
	v_pk_fma_f16 v8, v4, v146, v147 op_sel:[0,1,1] op_sel_hi:[1,1,1] neg_lo:[1,0,0] neg_hi:[1,0,0]
	v_pk_fma_f16 v9, v5, v146, v147 op_sel:[0,1,1] op_sel_hi:[1,1,1] neg_lo:[1,0,0] neg_hi:[1,0,0]
	v_mfma_f32_16x16x32_f16 v[22:25], v[10:13], v[2:5], 0
	ds_read2_b64 v[60:63], v32 offset0:19 offset1:221
	v_pk_fma_f16 v2, v100, v6, v2
	v_pk_fma_f16 v3, v101, v7, v3
	v_pk_fma_f16 v4, v102, v8, v4
	v_pk_fma_f16 v5, v103, v9, v5
	v_cndmask_b32_e64 v26, v26, v18, s[66:67]
	s_waitcnt lgkmcnt(7)
	v_pk_fma_f16 v6, v2, v148, v149 op_sel:[0,1,1] op_sel_hi:[1,1,1] neg_lo:[1,0,0] neg_hi:[1,0,0]
	v_pk_fma_f16 v7, v3, v148, v149 op_sel:[0,1,1] op_sel_hi:[1,1,1] neg_lo:[1,0,0] neg_hi:[1,0,0]
	v_pk_fma_f16 v8, v4, v148, v149 op_sel:[0,1,1] op_sel_hi:[1,1,1] neg_lo:[1,0,0] neg_hi:[1,0,0]
	v_pk_fma_f16 v9, v5, v148, v149 op_sel:[0,1,1] op_sel_hi:[1,1,1] neg_lo:[1,0,0] neg_hi:[1,0,0]
	v_mfma_f32_16x16x32_f16 v[18:21], v[10:13], v[2:5], 0
	ds_read2_b64 v[64:67], v32 offset0:20 offset1:222
	ds_read_b128 v[128:131], v33 offset:160
	v_pk_fma_f16 v2, v104, v6, v2
	v_pk_fma_f16 v3, v105, v7, v3
	v_pk_fma_f16 v4, v106, v8, v4
	v_pk_fma_f16 v5, v107, v9, v5
	v_cndmask_b32_e64 v27, v27, v23, s[66:67]
	v_pk_fma_f16 v6, v2, v150, v151 op_sel:[0,1,1] op_sel_hi:[1,1,1] neg_lo:[1,0,0] neg_hi:[1,0,0]
	v_pk_fma_f16 v7, v3, v150, v151 op_sel:[0,1,1] op_sel_hi:[1,1,1] neg_lo:[1,0,0] neg_hi:[1,0,0]
	v_pk_fma_f16 v8, v4, v150, v151 op_sel:[0,1,1] op_sel_hi:[1,1,1] neg_lo:[1,0,0] neg_hi:[1,0,0]
	v_pk_fma_f16 v9, v5, v150, v151 op_sel:[0,1,1] op_sel_hi:[1,1,1] neg_lo:[1,0,0] neg_hi:[1,0,0]
	v_mfma_f32_16x16x32_f16 v[22:25], v[10:13], v[2:5], 0
	ds_read2_b64 v[68:71], v32 offset0:21 offset1:223
	v_pk_fma_f16 v2, v108, v6, v2
	v_pk_fma_f16 v3, v109, v7, v3
	v_pk_fma_f16 v4, v110, v8, v4
	v_pk_fma_f16 v5, v111, v9, v5
	v_cndmask_b32_e64 v28, v28, v20, s[66:67]
	s_waitcnt lgkmcnt(6)
	v_pk_fma_f16 v6, v2, v120, v121 op_sel:[0,1,1] op_sel_hi:[1,1,1] neg_lo:[1,0,0] neg_hi:[1,0,0]
	v_pk_fma_f16 v7, v3, v120, v121 op_sel:[0,1,1] op_sel_hi:[1,1,1] neg_lo:[1,0,0] neg_hi:[1,0,0]
	v_pk_fma_f16 v8, v4, v120, v121 op_sel:[0,1,1] op_sel_hi:[1,1,1] neg_lo:[1,0,0] neg_hi:[1,0,0]
	v_pk_fma_f16 v9, v5, v120, v121 op_sel:[0,1,1] op_sel_hi:[1,1,1] neg_lo:[1,0,0] neg_hi:[1,0,0]
	v_mfma_f32_16x16x32_f16 v[18:21], v[14:17], v[2:5], 0
	ds_read2_b64 v[72:75], v32 offset0:22 offset1:224
	ds_read_b128 v[132:135], v33 offset:176
	ds_read_b32 v37, v36 offset:8
	ds_read_b32 v38, v36 offset:72
	v_pk_fma_f16 v2, v48, v6, v2
	v_pk_fma_f16 v3, v49, v7, v3
	v_pk_fma_f16 v4, v50, v8, v4
	v_pk_fma_f16 v5, v51, v9, v5
	v_cndmask_b32_e64 v29, v29, v25, s[66:67]
	v_cvt_pk_f16_f32 v30, v26, v27
	v_cvt_pk_f16_f32 v31, v28, v29
	ds_write_b16 v39, v30 offset:2048
	ds_write_b16_d16_hi v39, v30 offset:2112
	ds_write_b16 v39, v31 offset:2176
	ds_write_b16_d16_hi v39, v31 offset:2240
	s_mov_b64 exec, 1
	ds_add_u32 v36, v44 offset:128
	s_mov_b64 exec, -1
	v_pk_fma_f16 v6, v2, v122, v123 op_sel:[0,1,1] op_sel_hi:[1,1,1] neg_lo:[1,0,0] neg_hi:[1,0,0]
	v_pk_fma_f16 v7, v3, v122, v123 op_sel:[0,1,1] op_sel_hi:[1,1,1] neg_lo:[1,0,0] neg_hi:[1,0,0]
	v_pk_fma_f16 v8, v4, v122, v123 op_sel:[0,1,1] op_sel_hi:[1,1,1] neg_lo:[1,0,0] neg_hi:[1,0,0]
	v_pk_fma_f16 v9, v5, v122, v123 op_sel:[0,1,1] op_sel_hi:[1,1,1] neg_lo:[1,0,0] neg_hi:[1,0,0]
	v_mfma_f32_16x16x32_f16 v[22:25], v[14:17], v[2:5], 0
	ds_read2_b64 v[76:79], v32 offset0:23 offset1:225
	v_pk_fma_f16 v2, v52, v6, v2
	v_pk_fma_f16 v3, v53, v7, v3
	v_pk_fma_f16 v4, v54, v8, v4
	v_pk_fma_f16 v5, v55, v9, v5
	v_cndmask_b32_e64 v26, v26, v18, s[60:61]
	s_waitcnt lgkmcnt(13)
	v_pk_fma_f16 v6, v2, v124, v125 op_sel:[0,1,1] op_sel_hi:[1,1,1] neg_lo:[1,0,0] neg_hi:[1,0,0]
	v_pk_fma_f16 v7, v3, v124, v125 op_sel:[0,1,1] op_sel_hi:[1,1,1] neg_lo:[1,0,0] neg_hi:[1,0,0]
	v_pk_fma_f16 v8, v4, v124, v125 op_sel:[0,1,1] op_sel_hi:[1,1,1] neg_lo:[1,0,0] neg_hi:[1,0,0]
	v_pk_fma_f16 v9, v5, v124, v125 op_sel:[0,1,1] op_sel_hi:[1,1,1] neg_lo:[1,0,0] neg_hi:[1,0,0]
	v_mfma_f32_16x16x32_f16 v[18:21], v[14:17], v[2:5], 0
	ds_read2_b64 v[80:83], v32 offset0:24 offset1:226
	ds_read_b128 v[136:139], v33 offset:192
	v_pk_fma_f16 v2, v56, v6, v2
	v_pk_fma_f16 v3, v57, v7, v3
	v_pk_fma_f16 v4, v58, v8, v4
	v_pk_fma_f16 v5, v59, v9, v5
	v_cndmask_b32_e64 v27, v27, v23, s[60:61]
	v_pk_fma_f16 v6, v2, v126, v127 op_sel:[0,1,1] op_sel_hi:[1,1,1] neg_lo:[1,0,0] neg_hi:[1,0,0]
	v_pk_fma_f16 v7, v3, v126, v127 op_sel:[0,1,1] op_sel_hi:[1,1,1] neg_lo:[1,0,0] neg_hi:[1,0,0]
	v_pk_fma_f16 v8, v4, v126, v127 op_sel:[0,1,1] op_sel_hi:[1,1,1] neg_lo:[1,0,0] neg_hi:[1,0,0]
	v_pk_fma_f16 v9, v5, v126, v127 op_sel:[0,1,1] op_sel_hi:[1,1,1] neg_lo:[1,0,0] neg_hi:[1,0,0]
	v_mfma_f32_16x16x32_f16 v[22:25], v[14:17], v[2:5], 0
	ds_read2_b64 v[84:87], v32 offset0:25 offset1:227
	v_pk_fma_f16 v2, v60, v6, v2
	v_pk_fma_f16 v3, v61, v7, v3
	v_pk_fma_f16 v4, v62, v8, v4
	v_pk_fma_f16 v5, v63, v9, v5
	v_cndmask_b32_e64 v28, v28, v20, s[60:61]
	s_waitcnt lgkmcnt(13)
	v_pk_fma_f16 v6, v2, v128, v129 op_sel:[0,1,1] op_sel_hi:[1,1,1] neg_lo:[1,0,0] neg_hi:[1,0,0]
	v_pk_fma_f16 v7, v3, v128, v129 op_sel:[0,1,1] op_sel_hi:[1,1,1] neg_lo:[1,0,0] neg_hi:[1,0,0]
	v_pk_fma_f16 v8, v4, v128, v129 op_sel:[0,1,1] op_sel_hi:[1,1,1] neg_lo:[1,0,0] neg_hi:[1,0,0]
	v_pk_fma_f16 v9, v5, v128, v129 op_sel:[0,1,1] op_sel_hi:[1,1,1] neg_lo:[1,0,0] neg_hi:[1,0,0]
	v_mfma_f32_16x16x32_f16 v[18:21], v[14:17], v[2:5], 0
	ds_read2_b64 v[88:91], v32 offset0:26 offset1:228
	ds_read_b128 v[140:143], v33 offset:208
	v_pk_fma_f16 v2, v64, v6, v2
	v_pk_fma_f16 v3, v65, v7, v3
	v_pk_fma_f16 v4, v66, v8, v4
	v_pk_fma_f16 v5, v67, v9, v5
	v_cndmask_b32_e64 v29, v29, v25, s[60:61]
	v_pk_fma_f16 v6, v2, v130, v131 op_sel:[0,1,1] op_sel_hi:[1,1,1] neg_lo:[1,0,0] neg_hi:[1,0,0]
	v_pk_fma_f16 v7, v3, v130, v131 op_sel:[0,1,1] op_sel_hi:[1,1,1] neg_lo:[1,0,0] neg_hi:[1,0,0]
	v_pk_fma_f16 v8, v4, v130, v131 op_sel:[0,1,1] op_sel_hi:[1,1,1] neg_lo:[1,0,0] neg_hi:[1,0,0]
	v_pk_fma_f16 v9, v5, v130, v131 op_sel:[0,1,1] op_sel_hi:[1,1,1] neg_lo:[1,0,0] neg_hi:[1,0,0]
	v_mfma_f32_16x16x32_f16 v[22:25], v[14:17], v[2:5], 0
	ds_read2_b64 v[92:95], v32 offset0:27 offset1:229
	v_pk_fma_f16 v2, v68, v6, v2
	v_pk_fma_f16 v3, v69, v7, v3
	v_pk_fma_f16 v4, v70, v8, v4
	v_pk_fma_f16 v5, v71, v9, v5
	v_cndmask_b32_e64 v26, v26, v18, s[62:63]
	s_waitcnt lgkmcnt(6)
	v_pk_fma_f16 v6, v2, v132, v133 op_sel:[0,1,1] op_sel_hi:[1,1,1] neg_lo:[1,0,0] neg_hi:[1,0,0]
	v_pk_fma_f16 v7, v3, v132, v133 op_sel:[0,1,1] op_sel_hi:[1,1,1] neg_lo:[1,0,0] neg_hi:[1,0,0]
	v_pk_fma_f16 v8, v4, v132, v133 op_sel:[0,1,1] op_sel_hi:[1,1,1] neg_lo:[1,0,0] neg_hi:[1,0,0]
	v_pk_fma_f16 v9, v5, v132, v133 op_sel:[0,1,1] op_sel_hi:[1,1,1] neg_lo:[1,0,0] neg_hi:[1,0,0]
	v_mfma_f32_16x16x32_f16 v[18:21], v[14:17], v[2:5], 0
	ds_read2_b64 v[96:99], v32 offset0:28 offset1:230
	ds_read_b128 v[144:147], v33 offset:224
	v_pk_fma_f16 v2, v72, v6, v2
	v_pk_fma_f16 v3, v73, v7, v3
	v_pk_fma_f16 v4, v74, v8, v4
	v_pk_fma_f16 v5, v75, v9, v5
	v_cndmask_b32_e64 v27, v27, v23, s[62:63]
	v_pk_fma_f16 v6, v2, v134, v135 op_sel:[0,1,1] op_sel_hi:[1,1,1] neg_lo:[1,0,0] neg_hi:[1,0,0]
	v_pk_fma_f16 v7, v3, v134, v135 op_sel:[0,1,1] op_sel_hi:[1,1,1] neg_lo:[1,0,0] neg_hi:[1,0,0]
	v_pk_fma_f16 v8, v4, v134, v135 op_sel:[0,1,1] op_sel_hi:[1,1,1] neg_lo:[1,0,0] neg_hi:[1,0,0]
	v_pk_fma_f16 v9, v5, v134, v135 op_sel:[0,1,1] op_sel_hi:[1,1,1] neg_lo:[1,0,0] neg_hi:[1,0,0]
	v_mfma_f32_16x16x32_f16 v[22:25], v[14:17], v[2:5], 0
	ds_read2_b64 v[100:103], v32 offset0:29 offset1:231
	v_pk_fma_f16 v2, v76, v6, v2
	v_pk_fma_f16 v3, v77, v7, v3
	v_pk_fma_f16 v4, v78, v8, v4
	v_pk_fma_f16 v5, v79, v9, v5
	v_cndmask_b32_e64 v28, v28, v20, s[62:63]
	s_waitcnt lgkmcnt(6)
	v_pk_fma_f16 v6, v2, v136, v137 op_sel:[0,1,1] op_sel_hi:[1,1,1] neg_lo:[1,0,0] neg_hi:[1,0,0]
	v_pk_fma_f16 v7, v3, v136, v137 op_sel:[0,1,1] op_sel_hi:[1,1,1] neg_lo:[1,0,0] neg_hi:[1,0,0]
	v_pk_fma_f16 v8, v4, v136, v137 op_sel:[0,1,1] op_sel_hi:[1,1,1] neg_lo:[1,0,0] neg_hi:[1,0,0]
	v_pk_fma_f16 v9, v5, v136, v137 op_sel:[0,1,1] op_sel_hi:[1,1,1] neg_lo:[1,0,0] neg_hi:[1,0,0]
	v_mfma_f32_16x16x32_f16 v[18:21], v[14:17], v[2:5], 0
	ds_read2_b64 v[104:107], v32 offset0:30 offset1:232
	ds_read_b128 v[148:151], v33 offset:240
	v_pk_fma_f16 v2, v80, v6, v2
	v_pk_fma_f16 v3, v81, v7, v3
	v_pk_fma_f16 v4, v82, v8, v4
	v_pk_fma_f16 v5, v83, v9, v5
	v_cndmask_b32_e64 v29, v29, v25, s[62:63]
	v_readfirstlane_b32 s4, v37
	v_readfirstlane_b32 s5, v38
	s_and_b32 s4, s4, s5
	s_cbranch_scc0 .Lc1_slow1

.Lc1_nd1:
	v_pk_fma_f16 v6, v2, v138, v139 op_sel:[0,1,1] op_sel_hi:[1,1,1] neg_lo:[1,0,0] neg_hi:[1,0,0]
	v_pk_fma_f16 v7, v3, v138, v139 op_sel:[0,1,1] op_sel_hi:[1,1,1] neg_lo:[1,0,0] neg_hi:[1,0,0]
	v_pk_fma_f16 v8, v4, v138, v139 op_sel:[0,1,1] op_sel_hi:[1,1,1] neg_lo:[1,0,0] neg_hi:[1,0,0]
	v_pk_fma_f16 v9, v5, v138, v139 op_sel:[0,1,1] op_sel_hi:[1,1,1] neg_lo:[1,0,0] neg_hi:[1,0,0]
	v_mfma_f32_16x16x32_f16 v[22:25], v[14:17], v[2:5], 0
	ds_read2_b64 v[108:111], v32 offset0:31 offset1:233
	v_pk_fma_f16 v2, v84, v6, v2
	v_pk_fma_f16 v3, v85, v7, v3
	v_pk_fma_f16 v4, v86, v8, v4
	v_pk_fma_f16 v5, v87, v9, v5
	v_cndmask_b32_e64 v26, v26, v18, s[64:65]
	s_waitcnt lgkmcnt(6)
	v_pk_fma_f16 v6, v2, v140, v141 op_sel:[0,1,1] op_sel_hi:[1,1,1] neg_lo:[1,0,0] neg_hi:[1,0,0]
	v_pk_fma_f16 v7, v3, v140, v141 op_sel:[0,1,1] op_sel_hi:[1,1,1] neg_lo:[1,0,0] neg_hi:[1,0,0]
	v_pk_fma_f16 v8, v4, v140, v141 op_sel:[0,1,1] op_sel_hi:[1,1,1] neg_lo:[1,0,0] neg_hi:[1,0,0]
	v_pk_fma_f16 v9, v5, v140, v141 op_sel:[0,1,1] op_sel_hi:[1,1,1] neg_lo:[1,0,0] neg_hi:[1,0,0]
	v_mfma_f32_16x16x32_f16 v[18:21], v[14:17], v[2:5], 0
	ds_read2_b64 v[48:51], v32 offset0:32 offset1:234
	ds_read_b128 v[120:123], v33 offset:256
	ds_read2_b64 v[10:13], v34 offset0:32 offset1:234
	v_pk_fma_f16 v2, v88, v6, v2
	v_pk_fma_f16 v3, v89, v7, v3
	v_pk_fma_f16 v4, v90, v8, v4
	v_pk_fma_f16 v5, v91, v9, v5
	v_cndmask_b32_e64 v27, v27, v23, s[64:65]
	v_pk_fma_f16 v6, v2, v142, v143 op_sel:[0,1,1] op_sel_hi:[1,1,1] neg_lo:[1,0,0] neg_hi:[1,0,0]
	v_pk_fma_f16 v7, v3, v142, v143 op_sel:[0,1,1] op_sel_hi:[1,1,1] neg_lo:[1,0,0] neg_hi:[1,0,0]
	v_pk_fma_f16 v8, v4, v142, v143 op_sel:[0,1,1] op_sel_hi:[1,1,1] neg_lo:[1,0,0] neg_hi:[1,0,0]
	v_pk_fma_f16 v9, v5, v142, v143 op_sel:[0,1,1] op_sel_hi:[1,1,1] neg_lo:[1,0,0] neg_hi:[1,0,0]
	v_mfma_f32_16x16x32_f16 v[22:25], v[14:17], v[2:5], 0
	ds_read2_b64 v[52:55], v32 offset0:33 offset1:235
	v_pk_fma_f16 v2, v92, v6, v2
	v_pk_fma_f16 v3, v93, v7, v3
	v_pk_fma_f16 v4, v94, v8, v4
	v_pk_fma_f16 v5, v95, v9, v5
	v_cndmask_b32_e64 v28, v28, v20, s[64:65]
	s_waitcnt lgkmcnt(7)
	v_pk_fma_f16 v6, v2, v144, v145 op_sel:[0,1,1] op_sel_hi:[1,1,1] neg_lo:[1,0,0] neg_hi:[1,0,0]
	v_pk_fma_f16 v7, v3, v144, v145 op_sel:[0,1,1] op_sel_hi:[1,1,1] neg_lo:[1,0,0] neg_hi:[1,0,0]
	v_pk_fma_f16 v8, v4, v144, v145 op_sel:[0,1,1] op_sel_hi:[1,1,1] neg_lo:[1,0,0] neg_hi:[1,0,0]
	v_pk_fma_f16 v9, v5, v144, v145 op_sel:[0,1,1] op_sel_hi:[1,1,1] neg_lo:[1,0,0] neg_hi:[1,0,0]
	v_mfma_f32_16x16x32_f16 v[18:21], v[14:17], v[2:5], 0
	ds_read2_b64 v[56:59], v32 offset0:34 offset1:236
	ds_read_b128 v[124:127], v33 offset:272
	v_pk_fma_f16 v2, v96, v6, v2
	v_pk_fma_f16 v3, v97, v7, v3
	v_pk_fma_f16 v4, v98, v8, v4
	v_pk_fma_f16 v5, v99, v9, v5
	v_cndmask_b32_e64 v29, v29, v25, s[64:65]
	s_cmp_eq_u32 s72, 1
	s_cbranch_scc0 .Lc1_ns1
	s_waitcnt lgkmcnt(7)
	v_readfirstlane_b32 s4, v45
	s_cmp_eq_u32 s4, 4
	s_cbranch_scc0 .Lc1_dslow1

.Lc1_ns1:
	v_pk_fma_f16 v6, v2, v146, v147 op_sel:[0,1,1] op_sel_hi:[1,1,1] neg_lo:[1,0,0] neg_hi:[1,0,0]
	v_pk_fma_f16 v7, v3, v146, v147 op_sel:[0,1,1] op_sel_hi:[1,1,1] neg_lo:[1,0,0] neg_hi:[1,0,0]
	v_pk_fma_f16 v8, v4, v146, v147 op_sel:[0,1,1] op_sel_hi:[1,1,1] neg_lo:[1,0,0] neg_hi:[1,0,0]
	v_pk_fma_f16 v9, v5, v146, v147 op_sel:[0,1,1] op_sel_hi:[1,1,1] neg_lo:[1,0,0] neg_hi:[1,0,0]
	v_mfma_f32_16x16x32_f16 v[22:25], v[14:17], v[2:5], 0
	ds_read2_b64 v[60:63], v32 offset0:35 offset1:237
	v_pk_fma_f16 v2, v100, v6, v2
	v_pk_fma_f16 v3, v101, v7, v3
	v_pk_fma_f16 v4, v102, v8, v4
	v_pk_fma_f16 v5, v103, v9, v5
	v_cndmask_b32_e64 v26, v26, v18, s[66:67]
	s_waitcnt lgkmcnt(7)
	v_pk_fma_f16 v6, v2, v148, v149 op_sel:[0,1,1] op_sel_hi:[1,1,1] neg_lo:[1,0,0] neg_hi:[1,0,0]
	v_pk_fma_f16 v7, v3, v148, v149 op_sel:[0,1,1] op_sel_hi:[1,1,1] neg_lo:[1,0,0] neg_hi:[1,0,0]
	v_pk_fma_f16 v8, v4, v148, v149 op_sel:[0,1,1] op_sel_hi:[1,1,1] neg_lo:[1,0,0] neg_hi:[1,0,0]
	v_pk_fma_f16 v9, v5, v148, v149 op_sel:[0,1,1] op_sel_hi:[1,1,1] neg_lo:[1,0,0] neg_hi:[1,0,0]
	v_mfma_f32_16x16x32_f16 v[18:21], v[14:17], v[2:5], 0
	ds_read2_b64 v[64:67], v32 offset0:36 offset1:238
	ds_read_b128 v[128:131], v33 offset:288
	v_pk_fma_f16 v2, v104, v6, v2
	v_pk_fma_f16 v3, v105, v7, v3
	v_pk_fma_f16 v4, v106, v8, v4
	v_pk_fma_f16 v5, v107, v9, v5
	v_cndmask_b32_e64 v27, v27, v23, s[66:67]
	v_pk_fma_f16 v6, v2, v150, v151 op_sel:[0,1,1] op_sel_hi:[1,1,1] neg_lo:[1,0,0] neg_hi:[1,0,0]
	v_pk_fma_f16 v7, v3, v150, v151 op_sel:[0,1,1] op_sel_hi:[1,1,1] neg_lo:[1,0,0] neg_hi:[1,0,0]
	v_pk_fma_f16 v8, v4, v150, v151 op_sel:[0,1,1] op_sel_hi:[1,1,1] neg_lo:[1,0,0] neg_hi:[1,0,0]
	v_pk_fma_f16 v9, v5, v150, v151 op_sel:[0,1,1] op_sel_hi:[1,1,1] neg_lo:[1,0,0] neg_hi:[1,0,0]
	v_mfma_f32_16x16x32_f16 v[22:25], v[14:17], v[2:5], 0
	ds_read2_b64 v[68:71], v32 offset0:37 offset1:239
	v_pk_fma_f16 v2, v108, v6, v2
	v_pk_fma_f16 v3, v109, v7, v3
	v_pk_fma_f16 v4, v110, v8, v4
	v_pk_fma_f16 v5, v111, v9, v5
	v_cndmask_b32_e64 v28, v28, v20, s[66:67]
	v_add_u32_e32 v32, 0x100, v32
	v_add_u32_e32 v33, 0x100, v33
	v_add_u32_e32 v34, 0x100, v34
	v_add_u32_e32 v36, 8, v36
	v_add_u32_e32 v39, 0x1000, v39
	v_add_u32_e32 v43, 0x1000, v43
	v_add_u32_e32 v35, 0x800, v35
	s_xor_b32 s71, s71, 2
	s_add_i32 s70, s70, 1
	s_cmp_lt_u32 s70, 6
	s_cbranch_scc1 .Lc1_loop
	s_waitcnt lgkmcnt(6)
	v_pk_fma_f16 v6, v2, v120, v121 op_sel:[0,1,1] op_sel_hi:[1,1,1] neg_lo:[1,0,0] neg_hi:[1,0,0]
	v_pk_fma_f16 v7, v3, v120, v121 op_sel:[0,1,1] op_sel_hi:[1,1,1] neg_lo:[1,0,0] neg_hi:[1,0,0]
	v_pk_fma_f16 v8, v4, v120, v121 op_sel:[0,1,1] op_sel_hi:[1,1,1] neg_lo:[1,0,0] neg_hi:[1,0,0]
	v_pk_fma_f16 v9, v5, v120, v121 op_sel:[0,1,1] op_sel_hi:[1,1,1] neg_lo:[1,0,0] neg_hi:[1,0,0]
	v_mfma_f32_16x16x32_f16 v[18:21], v[10:13], v[2:5], 0
	ds_read2_b64 v[72:75], v32 offset0:6 offset1:208
	ds_read_b128 v[132:135], v33 offset:48
	v_pk_fma_f16 v2, v48, v6, v2
	v_pk_fma_f16 v3, v49, v7, v3
	v_pk_fma_f16 v4, v50, v8, v4
	v_pk_fma_f16 v5, v51, v9, v5
	v_cndmask_b32_e64 v29, v29, v25, s[66:67]
	v_cvt_pk_f16_f32 v30, v26, v27
	v_cvt_pk_f16_f32 v31, v28, v29
	ds_write_b16 v39, v30 offset:0
	ds_write_b16_d16_hi v39, v30 offset:64
	ds_write_b16 v39, v31 offset:128
	ds_write_b16_d16_hi v39, v31 offset:192
	s_mov_b64 exec, 1
	ds_add_u32 v36, v44 offset:124
	s_mov_b64 exec, -1
	v_pk_fma_f16 v6, v2, v122, v123 op_sel:[0,1,1] op_sel_hi:[1,1,1] neg_lo:[1,0,0] neg_hi:[1,0,0]
	v_pk_fma_f16 v7, v3, v122, v123 op_sel:[0,1,1] op_sel_hi:[1,1,1] neg_lo:[1,0,0] neg_hi:[1,0,0]
	v_pk_fma_f16 v8, v4, v122, v123 op_sel:[0,1,1] op_sel_hi:[1,1,1] neg_lo:[1,0,0] neg_hi:[1,0,0]
	v_pk_fma_f16 v9, v5, v122, v123 op_sel:[0,1,1] op_sel_hi:[1,1,1] neg_lo:[1,0,0] neg_hi:[1,0,0]
	v_mfma_f32_16x16x32_f16 v[22:25], v[10:13], v[2:5], 0
	ds_read2_b64 v[76:79], v32 offset0:7 offset1:209
	v_pk_fma_f16 v2, v52, v6, v2
	v_pk_fma_f16 v3, v53, v7, v3
	v_pk_fma_f16 v4, v54, v8, v4
	v_pk_fma_f16 v5, v55, v9, v5
	v_cndmask_b32_e64 v26, v26, v18, s[60:61]
	s_waitcnt lgkmcnt(11)
	v_pk_fma_f16 v6, v2, v124, v125 op_sel:[0,1,1] op_sel_hi:[1,1,1] neg_lo:[1,0,0] neg_hi:[1,0,0]
	v_pk_fma_f16 v7, v3, v124, v125 op_sel:[0,1,1] op_sel_hi:[1,1,1] neg_lo:[1,0,0] neg_hi:[1,0,0]
	v_pk_fma_f16 v8, v4, v124, v125 op_sel:[0,1,1] op_sel_hi:[1,1,1] neg_lo:[1,0,0] neg_hi:[1,0,0]
	v_pk_fma_f16 v9, v5, v124, v125 op_sel:[0,1,1] op_sel_hi:[1,1,1] neg_lo:[1,0,0] neg_hi:[1,0,0]
	v_mfma_f32_16x16x32_f16 v[18:21], v[10:13], v[2:5], 0
	v_pk_fma_f16 v2, v56, v6, v2
	v_pk_fma_f16 v3, v57, v7, v3
	v_pk_fma_f16 v4, v58, v8, v4
	v_pk_fma_f16 v5, v59, v9, v5
	v_cndmask_b32_e64 v27, v27, v23, s[60:61]
	v_pk_fma_f16 v6, v2, v126, v127 op_sel:[0,1,1] op_sel_hi:[1,1,1] neg_lo:[1,0,0] neg_hi:[1,0,0]
	v_pk_fma_f16 v7, v3, v126, v127 op_sel:[0,1,1] op_sel_hi:[1,1,1] neg_lo:[1,0,0] neg_hi:[1,0,0]
	v_pk_fma_f16 v8, v4, v126, v127 op_sel:[0,1,1] op_sel_hi:[1,1,1] neg_lo:[1,0,0] neg_hi:[1,0,0]
	v_pk_fma_f16 v9, v5, v126, v127 op_sel:[0,1,1] op_sel_hi:[1,1,1] neg_lo:[1,0,0] neg_hi:[1,0,0]
	v_mfma_f32_16x16x32_f16 v[22:25], v[10:13], v[2:5], 0
	v_pk_fma_f16 v2, v60, v6, v2
	v_pk_fma_f16 v3, v61, v7, v3
	v_pk_fma_f16 v4, v62, v8, v4
	v_pk_fma_f16 v5, v63, v9, v5
	v_cndmask_b32_e64 v28, v28, v20, s[60:61]
	s_waitcnt lgkmcnt(8)
	s_mov_b32 s72, 0
	s_cmp_eq_u32 s70, 0
	s_cbranch_scc1 .Lc1_ndt
	s_sub_i32 s4, 3, s71
	s_cmp_eq_u32 s36, s4
	s_cbranch_scc0 .Lc1_ndt
	s_mov_b32 s72, 1
	ds_read_b32 v45, v36 offset:124
	ds_read_b128 v[112:115], v43 offset:0
	ds_read_b128 v[116:119], v43 offset:1024
.Lc1_ndt:
	v_pk_fma_f16 v6, v2, v128, v129 op_sel:[0,1,1] op_sel_hi:[1,1,1] neg_lo:[1,0,0] neg_hi:[1,0,0]
	v_pk_fma_f16 v7, v3, v128, v129 op_sel:[0,1,1] op_sel_hi:[1,1,1] neg_lo:[1,0,0] neg_hi:[1,0,0]
	v_pk_fma_f16 v8, v4, v128, v129 op_sel:[0,1,1] op_sel_hi:[1,1,1] neg_lo:[1,0,0] neg_hi:[1,0,0]
	v_pk_fma_f16 v9, v5, v128, v129 op_sel:[0,1,1] op_sel_hi:[1,1,1] neg_lo:[1,0,0] neg_hi:[1,0,0]
	v_mfma_f32_16x16x32_f16 v[18:21], v[10:13], v[2:5], 0
	v_pk_fma_f16 v2, v64, v6, v2
	v_pk_fma_f16 v3, v65, v7, v3
	v_pk_fma_f16 v4, v66, v8, v4
	v_pk_fma_f16 v5, v67, v9, v5
	v_cndmask_b32_e64 v29, v29, v25, s[60:61]
	v_pk_fma_f16 v6, v2, v130, v131 op_sel:[0,1,1] op_sel_hi:[1,1,1] neg_lo:[1,0,0] neg_hi:[1,0,0]
	v_pk_fma_f16 v7, v3, v130, v131 op_sel:[0,1,1] op_sel_hi:[1,1,1] neg_lo:[1,0,0] neg_hi:[1,0,0]
	v_pk_fma_f16 v8, v4, v130, v131 op_sel:[0,1,1] op_sel_hi:[1,1,1] neg_lo:[1,0,0] neg_hi:[1,0,0]
	v_pk_fma_f16 v9, v5, v130, v131 op_sel:[0,1,1] op_sel_hi:[1,1,1] neg_lo:[1,0,0] neg_hi:[1,0,0]
	v_mfma_f32_16x16x32_f16 v[22:25], v[10:13], v[2:5], 0
	v_pk_fma_f16 v2, v68, v6, v2
	v_pk_fma_f16 v3, v69, v7, v3
	v_pk_fma_f16 v4, v70, v8, v4
	v_pk_fma_f16 v5, v71, v9, v5
	v_cndmask_b32_e64 v26, v26, v18, s[62:63]
	s_waitcnt lgkmcnt(0)
	v_pk_fma_f16 v6, v2, v132, v133 op_sel:[0,1,1] op_sel_hi:[1,1,1] neg_lo:[1,0,0] neg_hi:[1,0,0]
	v_pk_fma_f16 v7, v3, v132, v133 op_sel:[0,1,1] op_sel_hi:[1,1,1] neg_lo:[1,0,0] neg_hi:[1,0,0]
	v_pk_fma_f16 v8, v4, v132, v133 op_sel:[0,1,1] op_sel_hi:[1,1,1] neg_lo:[1,0,0] neg_hi:[1,0,0]
	v_pk_fma_f16 v9, v5, v132, v133 op_sel:[0,1,1] op_sel_hi:[1,1,1] neg_lo:[1,0,0] neg_hi:[1,0,0]
	v_mfma_f32_16x16x32_f16 v[18:21], v[10:13], v[2:5], 0
	v_pk_fma_f16 v2, v72, v6, v2
	v_pk_fma_f16 v3, v73, v7, v3
	v_pk_fma_f16 v4, v74, v8, v4
	v_pk_fma_f16 v5, v75, v9, v5
	v_cndmask_b32_e64 v27, v27, v23, s[62:63]
	s_cmp_eq_u32 s72, 1
	s_cbranch_scc0 .Lc1_nst
	s_waitcnt lgkmcnt(0)
	v_readfirstlane_b32 s4, v45
	s_cmp_eq_u32 s4, 4
	s_cbranch_scc0 .Lc1_dslowt

.Lc1_nst:
	v_pk_fma_f16 v6, v2, v134, v135 op_sel:[0,1,1] op_sel_hi:[1,1,1] neg_lo:[1,0,0] neg_hi:[1,0,0]
	v_pk_fma_f16 v7, v3, v134, v135 op_sel:[0,1,1] op_sel_hi:[1,1,1] neg_lo:[1,0,0] neg_hi:[1,0,0]
	v_pk_fma_f16 v8, v4, v134, v135 op_sel:[0,1,1] op_sel_hi:[1,1,1] neg_lo:[1,0,0] neg_hi:[1,0,0]
	v_pk_fma_f16 v9, v5, v134, v135 op_sel:[0,1,1] op_sel_hi:[1,1,1] neg_lo:[1,0,0] neg_hi:[1,0,0]
	v_mfma_f32_16x16x32_f16 v[22:25], v[10:13], v[2:5], 0
	v_pk_fma_f16 v2, v76, v6, v2
	v_pk_fma_f16 v3, v77, v7, v3
	v_pk_fma_f16 v4, v78, v8, v4
	v_pk_fma_f16 v5, v79, v9, v5
	v_cndmask_b32_e64 v28, v28, v20, s[62:63]
	s_nop 7
	v_cndmask_b32_e64 v29, v29, v25, s[62:63]
	v_cvt_pk_f16_f32 v30, v26, v27
	v_cvt_pk_f16_f32 v31, v28, v29
	ds_write_b16 v39, v30 offset:2048
	ds_write_b16_d16_hi v39, v30 offset:2112
	ds_write_b16 v39, v31 offset:2176
	ds_write_b16_d16_hi v39, v31 offset:2240
	s_mov_b64 exec, 1
	ds_add_u32 v36, v44 offset:128
	s_mov_b64 exec, -1
	s_cmp_eq_u32 s36, 0
	s_cbranch_scc0 .Lc1_end

	.amdhsa_kernel _Z2kA5AArgs
		.amdhsa_group_segment_fixed_size 113408
		.amdhsa_private_segment_fixed_size 0
		.amdhsa_kernarg_size 120
		.amdhsa_user_sgpr_count 2
		.amdhsa_user_sgpr_dispatch_ptr 0
		.amdhsa_user_sgpr_queue_ptr 0
		.amdhsa_user_sgpr_kernarg_segment_ptr 1
		.amdhsa_user_sgpr_dispatch_id 0
		.amdhsa_user_sgpr_kernarg_preload_length 0
		.amdhsa_user_sgpr_kernarg_preload_offset 0
		.amdhsa_user_sgpr_private_segment_size 0
		.amdhsa_uses_dynamic_stack 0
		.amdhsa_enable_private_segment 0
		.amdhsa_system_sgpr_workgroup_id_x 1
		.amdhsa_system_sgpr_workgroup_id_y 0
		.amdhsa_system_sgpr_workgroup_id_z 0
		.amdhsa_system_sgpr_workgroup_info 0
		.amdhsa_system_vgpr_workitem_id 0
		.amdhsa_next_free_vgpr 224
		.amdhsa_next_free_sgpr 96
		.amdhsa_accum_offset 224
		.amdhsa_reserve_vcc 1
		.amdhsa_float_round_mode_32 0
		.amdhsa_float_round_mode_16_64 0
		.amdhsa_float_denorm_mode_32 3
		.amdhsa_float_denorm_mode_16_64 3
		.amdhsa_dx10_clamp 1
		.amdhsa_ieee_mode 1
		.amdhsa_fp16_overflow 0
		.amdhsa_tg_split 0
		.amdhsa_exception_fp_ieee_invalid_op 0
		.amdhsa_exception_fp_denorm_src 0
		.amdhsa_exception_fp_ieee_div_zero 0
		.amdhsa_exception_fp_ieee_overflow 0
		.amdhsa_exception_fp_ieee_underflow 0
		.amdhsa_exception_fp_ieee_inexact 0
		.amdhsa_exception_int_div_zero 0
	.end_amdhsa_kernel

amdhsa.kernels:
  - .agpr_count:     0
    .args:
      - .offset:         0
        .size:           120
        .value_kind:     by_value
    .group_segment_fixed_size: 113408
    .kernarg_segment_align: 8
    .kernarg_segment_size: 120
    .language:       OpenCL C
    .language_version:
      - 2
      - 0
    .max_flat_workgroup_size: 512
    .name:           _Z2kA5AArgs
    .private_segment_fixed_size: 0
    .sgpr_count:     50
    .sgpr_spill_count: 0
    .symbol:         _Z2kA5AArgs.kd
    .uniform_work_group_size: 1
    .uses_dynamic_stack: false
    .vgpr_count:     224
    .vgpr_spill_count: 0
    .wavefront_size: 64
  - .agpr_count:     0
    .args:
      - .actual_access:  read_only
        .address_space:  global
        .offset:         0
        .size:           8
        .value_kind:     global_buffer
      - .actual_access:  read_only
        .address_space:  global
        .offset:         8
        .size:           8
        .value_kind:     global_buffer
      - .actual_access:  read_only
        .address_space:  global
        .offset:         16
        .size:           8
        .value_kind:     global_buffer
      - .actual_access:  read_only
        .address_space:  global
        .offset:         24
        .size:           8
        .value_kind:     global_buffer
      - .actual_access:  read_only
        .address_space:  global
        .offset:         32
        .size:           8
        .value_kind:     global_buffer
      - .actual_access:  read_only
        .address_space:  global
        .offset:         40
        .size:           8
        .value_kind:     global_buffer
      - .actual_access:  write_only
        .address_space:  global
        .offset:         48
        .size:           8
        .value_kind:     global_buffer
    .group_segment_fixed_size: 65792
    .kernarg_segment_align: 8
    .kernarg_segment_size: 56
    .language:       OpenCL C
    .language_version:
      - 2
      - 0
    .max_flat_workgroup_size: 512
    .name:           _Z2kBPKfPKDv4_jPKDF16_S0_S0_S0_Pf
    .private_segment_fixed_size: 0
    .sgpr_count:     18
    .sgpr_spill_count: 0
    .symbol:         _Z2kBPKfPKDv4_jPKDF16_S0_S0_S0_Pf.kd
    .uniform_work_group_size: 1
    .uses_dynamic_stack: false
    .vgpr_count:     109
    .vgpr_spill_count: 0
    .wavefront_size: 64
